# speedup vs baseline: 1.0202x; 1.0202x over previous
.LBB2_37:
	v_cvt_f32_u32_e32 v1, s26
	s_lshl_b32 s3, s22, 1
	s_sub_i32 s9, 0, s26
	s_sub_i32 s3, s18, s3
	v_rcp_iflag_f32_e32 v1, v1
	s_add_i32 s8, s17, -1
	s_add_i32 s12, s8, s26
	s_ashr_i32 s15, s12, 31
	v_mul_f32_e32 v1, 0x4f7ffffe, v1
	v_cvt_u32_f32_e32 v1, v1
	s_abs_i32 s12, s12
	v_lshrrev_b32_e32 v2, 3, v0
	s_mov_b32 s13, 0
	v_readfirstlane_b32 s18, v1
	s_mul_i32 s9, s9, s18
	s_mul_hi_u32 s9, s18, s9
	s_add_i32 s18, s18, s9
	s_mul_hi_u32 s9, s12, s18
	s_mul_i32 s18, s9, s26
	s_sub_i32 s12, s12, s18
	s_add_i32 s19, s9, 1
	s_sub_i32 s18, s12, s26
	s_cmp_ge_u32 s12, s26
	s_cselect_b32 s9, s19, s9
	s_cselect_b32 s12, s18, s12
	s_add_i32 s18, s9, 1
	s_cmp_ge_u32 s12, s26
	s_cselect_b32 s9, s18, s9
	s_xor_b32 s9, s9, s15
	s_sub_i32 s19, s9, s15
	s_add_i32 s19, s19, 15
	s_and_b32 s20, s19, -16
	s_mul_i32 s22, s20, s2
	s_lshl_b32 s33, s3, 8
	v_add_u32_e32 v5, s22, v2
	s_ashr_i32 s18, s33, 31
	s_add_i32 s21, s16, 0x1fff
	v_min_i32_e32 v10, s8, v5
	s_lshl_b32 s12, s14, 9
	v_or_b32_e32 v6, s33, v2
	v_mov_b32_e32 v7, s18
	v_sub_u32_e32 v11, s21, v10
	v_cmp_gt_i32_e32 vcc, s16, v10
	v_lshl_add_u64 v[6:7], v[6:7], 0, s[12:13]
	s_lshl_b32 s13, s14, 13
	v_cndmask_b32_e32 v10, v11, v10, vcc
	v_add_u32_e32 v10, s13, v10
	v_ashrrev_i32_e32 v11, 31, v10
	s_waitcnt lgkmcnt(0)
	v_lshl_add_u64 v[10:11], v[10:11], 2, s[10:11]
	global_load_dword v16, v[10:11], off
	v_add_u32_e32 v10, 64, v5
	v_min_i32_e32 v10, s8, v10
	v_sub_u32_e32 v11, s21, v10
	v_cmp_gt_i32_e32 vcc, s16, v10
	v_xor_b32_e32 v4, v2, v0
	v_lshlrev_b32_e32 v1, 4, v4
	v_cndmask_b32_e32 v10, v11, v10, vcc
	v_add_u32_e32 v10, s13, v10
	v_ashrrev_i32_e32 v11, 31, v10
	v_lshl_add_u64 v[10:11], v[10:11], 2, s[10:11]
	global_load_dword v17, v[10:11], off
	v_and_b32_e32 v10, 0x70, v1
	v_add_u32_e32 v1, 0x80, v5
	v_min_i32_e32 v1, s8, v1
	v_sub_u32_e32 v5, s21, v1
	v_cmp_gt_i32_e32 vcc, s16, v1
	v_mov_b32_e32 v3, 0
	v_lshlrev_b64 v[6:7], 11, v[6:7]
	v_cndmask_b32_e32 v1, v5, v1, vcc
	v_add_u32_e32 v14, s13, v1
	v_lshl_add_u64 v[8:9], s[6:7], 0, v[6:7]
	v_mov_b32_e32 v11, v3
	v_ashrrev_i32_e32 v15, 31, v14
	v_lshlrev_b32_e32 v1, 4, v0
	v_lshl_add_u64 v[8:9], v[8:9], 0, v[10:11]
	s_mov_b64 s[2:3], 0x20000
	v_or_b32_e32 v6, 0x40000, v6
	v_lshl_add_u64 v[14:15], v[14:15], 2, s[10:11]
	v_add_u32_e32 v187, 0, v1
	v_lshl_add_u64 v[12:13], v[8:9], 0, s[2:3]
	v_lshl_add_u64 v[6:7], s[6:7], 0, v[6:7]
	s_mov_b64 s[2:3], 0x60000
	global_load_dword v5, v[14:15], off
	v_add_u32_e32 v14, 0x4800, v187
	v_lshl_add_u64 v[222:223], v[6:7], 0, v[10:11]
	v_lshl_add_u64 v[6:7], v[8:9], 0, s[2:3]
	v_readfirstlane_b32 s2, v14
	v_add_u32_e32 v14, 0x6800, v187
	s_mov_b32 m0, s2
	v_readfirstlane_b32 s2, v14
	global_load_lds_dwordx4 v[8:9], off
	s_mov_b32 m0, s2
	v_readfirstlane_b32 s23, v0
	global_load_lds_dwordx4 v[12:13], off
	v_add_u32_e32 v12, 0x8800, v187
	s_lshr_b32 s34, s23, 6
	v_readfirstlane_b32 s2, v12
	v_add_u32_e32 v12, 0xa800, v187
	s_mov_b32 m0, s2
	v_readfirstlane_b32 s2, v12
	global_load_lds_dwordx4 v[222:223], off
	s_mov_b32 m0, s2
	s_add_i32 s2, 0, 0x11000
	v_add_u32_e32 v189, s2, v1
	s_mov_b64 s[2:3], 0x80
	v_readfirstlane_b32 s8, v189
	global_load_lds_dwordx4 v[6:7], off
	v_lshl_add_u64 v[6:7], v[8:9], 0, s[2:3]
	s_mov_b32 m0, s8
	s_mov_b64 s[8:9], 0x20080
	v_add_u32_e32 v12, 0x2000, v189
	global_load_lds_dwordx4 v[6:7], off
	v_lshl_add_u64 v[6:7], v[8:9], 0, s[8:9]
	v_readfirstlane_b32 s8, v12
	v_add_u32_e32 v12, 0x4000, v189
	s_mov_b32 m0, s8
	v_readfirstlane_b32 s8, v12
	global_load_lds_dwordx4 v[6:7], off
	v_lshl_add_u64 v[6:7], v[222:223], 0, s[2:3]
	s_mov_b32 m0, s8
	s_mov_b64 s[8:9], 0x60080
	global_load_lds_dwordx4 v[6:7], off
	v_lshl_add_u64 v[6:7], v[8:9], 0, s[8:9]
	v_add_u32_e32 v8, 0x6000, v189
	s_waitcnt vmcnt(7)
	v_lshlrev_b32_e32 v5, 11, v5
	v_readfirstlane_b32 s8, v8
	s_mov_b32 m0, s8
	v_readfirstlane_b32 s8, v187
	global_load_lds_dwordx4 v[6:7], off
	v_lshlrev_b32_e32 v6, 11, v16
	v_and_b32_e32 v6, 0xfff800, v6
	v_mov_b32_e32 v7, v3
	v_lshl_add_u64 v[6:7], s[4:5], 0, v[6:7]
	v_lshl_add_u64 v[224:225], v[6:7], 0, v[10:11]
	v_lshlrev_b32_e32 v6, 11, v17
	v_and_b32_e32 v6, 0xfff800, v6
	v_mov_b32_e32 v7, v3
	v_lshl_add_u64 v[6:7], s[4:5], 0, v[6:7]
	v_lshl_add_u64 v[226:227], v[6:7], 0, v[10:11]
	v_add_u32_e32 v6, 0x2000, v187
	s_mov_b32 m0, s8
	v_readfirstlane_b32 s8, v6
	global_load_lds_dwordx4 v[224:225], off
	s_mov_b32 m0, s8
	s_lshr_b32 s8, s19, 3
	global_load_lds_dwordx4 v[226:227], off
	s_and_b32 s8, s8, 0x1ffffffe
	s_add_i32 s8, s8, -16
	v_and_b32_e32 v6, 0xfff800, v5
	v_mov_b32_e32 v7, v3
	s_cmp_lt_i32 s34, s8
	v_lshl_add_u64 v[6:7], s[4:5], 0, v[6:7]
	s_cselect_b64 s[4:5], -1, 0
	s_cmp_ge_i32 s34, s8
	s_cselect_b64 s[8:9], -1, 0
	v_lshl_add_u64 v[228:229], v[6:7], 0, v[10:11]
	s_and_b64 vcc, exec, s[8:9]
	s_cbranch_vccnz .LBB2_39
	v_add_u32_e32 v5, 0x4000, v187
	s_nop 0
	v_readfirstlane_b32 s14, v5
	s_mov_b32 m0, s14
	s_nop 0
	global_load_lds_dwordx4 v[228:229], off

.LBB2_81:
	ds_read_b128 v[110:113], v203 offset:18432
	ds_read_b128 v[114:117], v203 offset:20480
	ds_read_b128 v[38:41], v207
	ds_read_b128 v[42:45], v207 offset:2048
	ds_read_b128 v[232:235], v207 offset:4096
	ds_read_b128 v[236:239], v207 offset:6144
	s_and_b64 vcc, exec, s[0:1]
	s_waitcnt lgkmcnt(2)
	v_mfma_f32_16x16x32_f16 v[74:77], v[110:113], v[38:41], v[2:5]
	v_mfma_f32_16x16x32_f16 v[66:69], v[114:117], v[38:41], v[6:9]
	v_mfma_f32_16x16x32_f16 v[62:65], v[110:113], v[42:45], v[10:13]
	v_mfma_f32_16x16x32_f16 v[58:61], v[114:117], v[42:45], v[14:17]
	ds_read_b128 v[240:243], v207 offset:8192
	ds_read_b128 v[244:247], v207 offset:10240
	s_waitcnt lgkmcnt(2)
	v_mfma_f32_16x16x32_f16 v[54:57], v[110:113], v[232:235], v[18:21]
	v_mfma_f32_16x16x32_f16 v[50:53], v[114:117], v[232:235], v[22:25]
	v_mfma_f32_16x16x32_f16 v[46:49], v[110:113], v[236:239], v[26:29]
	v_mfma_f32_16x16x32_f16 v[42:45], v[114:117], v[236:239], v[30:33]
	ds_read_b128 v[232:235], v207 offset:12288
	ds_read_b128 v[236:239], v207 offset:14336
	s_waitcnt lgkmcnt(2)
	v_mfma_f32_16x16x32_f16 v[38:41], v[110:113], v[240:243], v[34:37]
	v_mfma_f32_16x16x32_f16 v[34:37], v[114:117], v[240:243], v[102:105]
	v_mfma_f32_16x16x32_f16 v[30:33], v[110:113], v[244:247], v[98:101]
	v_mfma_f32_16x16x32_f16 v[26:29], v[114:117], v[244:247], v[94:97]
	s_waitcnt lgkmcnt(0)
	v_mfma_f32_16x16x32_f16 v[22:25], v[110:113], v[232:235], v[90:93]
	v_mfma_f32_16x16x32_f16 v[18:21], v[114:117], v[232:235], v[86:89]
	v_mfma_f32_16x16x32_f16 v[14:17], v[110:113], v[236:239], v[106:109]
	v_mfma_f32_16x16x32_f16 v[10:13], v[114:117], v[236:239], v[82:85]
	s_cbranch_vccnz .LBB2_83
	ds_read_b128 v[2:5], v207 offset:16384
	s_waitcnt lgkmcnt(0)
	v_mfma_f32_16x16x32_f16 v[6:9], v[110:113], v[2:5], v[70:73]
	v_mfma_f32_16x16x32_f16 v[2:5], v[114:117], v[2:5], v[78:81]
	s_andn2_b64 vcc, exec, s[30:31]
	s_mov_b64 s[30:31], -1
	s_cbranch_vccnz .LBB2_67
	s_branch .LBB2_84

.LBB2_95:
	v_add_u32_e32 v70, 0, v195
	ds_read_b128 v[146:149], v70 offset:51200
	ds_read_b128 v[150:153], v70 offset:53248
	ds_read_b128 v[70:73], v205 offset:51200
	ds_read_b128 v[78:81], v205 offset:53248
	ds_read_b128 v[232:235], v205 offset:55296
	ds_read_b128 v[236:239], v205 offset:57344
	s_and_b64 vcc, exec, s[0:1]
	s_waitcnt lgkmcnt(2)
	v_mfma_f32_16x16x32_f16 v[82:85], v[146:149], v[70:73], v[74:77]
	v_mfma_f32_16x16x32_f16 v[86:89], v[150:153], v[70:73], v[66:69]
	v_mfma_f32_16x16x32_f16 v[90:93], v[146:149], v[78:81], v[62:65]
	v_mfma_f32_16x16x32_f16 v[94:97], v[150:153], v[78:81], v[58:61]
	ds_read_b128 v[240:243], v205 offset:59392
	ds_read_b128 v[244:247], v205 offset:61440
	s_waitcnt lgkmcnt(2)
	v_mfma_f32_16x16x32_f16 v[98:101], v[146:149], v[232:235], v[54:57]
	v_mfma_f32_16x16x32_f16 v[102:105], v[150:153], v[232:235], v[50:53]
	v_mfma_f32_16x16x32_f16 v[106:109], v[146:149], v[236:239], v[46:49]
	v_mfma_f32_16x16x32_f16 v[110:113], v[150:153], v[236:239], v[42:45]
	ds_read_b128 v[232:235], v205 offset:63488
	ds_read_b128 v[236:239], v209 offset:14336
	s_waitcnt lgkmcnt(2)
	v_mfma_f32_16x16x32_f16 v[114:117], v[146:149], v[240:243], v[38:41]
	v_mfma_f32_16x16x32_f16 v[118:121], v[150:153], v[240:243], v[34:37]
	v_mfma_f32_16x16x32_f16 v[122:125], v[146:149], v[244:247], v[30:33]
	v_mfma_f32_16x16x32_f16 v[126:129], v[150:153], v[244:247], v[26:29]
	v_mov_b64_e32 v[80:81], v[4:5]
	v_mov_b64_e32 v[78:79], v[2:3]
	s_waitcnt lgkmcnt(0)
	v_mfma_f32_16x16x32_f16 v[130:133], v[146:149], v[232:235], v[22:25]
	v_mfma_f32_16x16x32_f16 v[134:137], v[150:153], v[232:235], v[18:21]
	v_mov_b64_e32 v[72:73], v[8:9]
	v_mov_b64_e32 v[70:71], v[6:7]
	v_mfma_f32_16x16x32_f16 v[138:141], v[146:149], v[236:239], v[14:17]
	v_mfma_f32_16x16x32_f16 v[142:145], v[150:153], v[236:239], v[10:13]
	s_cbranch_vccnz .LBB2_97
	ds_read_b128 v[78:81], v209 offset:16384
	s_waitcnt lgkmcnt(0)
	v_mfma_f32_16x16x32_f16 v[70:73], v[146:149], v[78:81], v[6:9]
	v_mfma_f32_16x16x32_f16 v[78:81], v[150:153], v[78:81], v[2:5]
.LBB2_97:
	v_add_u32_e32 v150, 0, v199
	ds_read_b128 v[146:149], v150 offset:51200
	ds_read_b128 v[150:153], v150 offset:53248
	ds_read_b128 v[162:165], v207 offset:51200
	ds_read_b128 v[166:169], v207 offset:53248
	ds_read_b128 v[232:235], v207 offset:55296
	ds_read_b128 v[236:239], v207 offset:57344
	s_and_b64 vcc, exec, s[0:1]
	s_waitcnt lgkmcnt(2)
	v_mfma_f32_16x16x32_f16 v[82:85], v[146:149], v[162:165], v[82:85]
	v_mfma_f32_16x16x32_f16 v[86:89], v[150:153], v[162:165], v[86:89]
	v_mfma_f32_16x16x32_f16 v[90:93], v[146:149], v[166:169], v[90:93]
	v_mfma_f32_16x16x32_f16 v[94:97], v[150:153], v[166:169], v[94:97]
	ds_read_b128 v[162:165], v207 offset:59392
	ds_read_b128 v[166:169], v207 offset:61440
	s_waitcnt lgkmcnt(2)
	v_mfma_f32_16x16x32_f16 v[98:101], v[146:149], v[232:235], v[98:101]
	v_mfma_f32_16x16x32_f16 v[102:105], v[150:153], v[232:235], v[102:105]
	v_mfma_f32_16x16x32_f16 v[106:109], v[146:149], v[236:239], v[106:109]
	v_mfma_f32_16x16x32_f16 v[110:113], v[150:153], v[236:239], v[110:113]
	ds_read_b128 v[232:235], v207 offset:63488
	ds_read_b128 v[236:239], v211 offset:14336
	s_waitcnt lgkmcnt(2)
	v_mfma_f32_16x16x32_f16 v[114:117], v[146:149], v[162:165], v[114:117]
	v_mfma_f32_16x16x32_f16 v[118:121], v[150:153], v[162:165], v[118:121]
	v_mfma_f32_16x16x32_f16 v[122:125], v[146:149], v[166:169], v[122:125]
	v_mfma_f32_16x16x32_f16 v[126:129], v[150:153], v[166:169], v[126:129]
	s_waitcnt lgkmcnt(0)
	v_mfma_f32_16x16x32_f16 v[130:133], v[146:149], v[232:235], v[130:133]
	v_mfma_f32_16x16x32_f16 v[134:137], v[150:153], v[232:235], v[134:137]
	v_mfma_f32_16x16x32_f16 v[138:141], v[146:149], v[236:239], v[138:141]
	v_mfma_f32_16x16x32_f16 v[142:145], v[150:153], v[236:239], v[142:145]
	s_cbranch_vccnz .LBB2_108
	ds_read_b128 v[162:165], v211 offset:16384
	s_waitcnt lgkmcnt(0)
	v_mfma_f32_16x16x32_f16 v[70:73], v[146:149], v[162:165], v[70:73]
	v_mfma_f32_16x16x32_f16 v[78:81], v[150:153], v[162:165], v[78:81]
	s_cmpk_lg_i32 s6, 0x680
	s_mov_b64 s[30:31], -1
	s_cbranch_scc1 .LBB2_109

.LBB2_104:
	v_add_u32_e32 v146, s37, v195
	ds_read_b128 v[178:181], v146
	v_add_u32_e32 v213, s37, v193
	ds_read_b128 v[182:185], v146 offset:2048
	ds_read_b128 v[146:149], v213
	ds_read_b128 v[150:153], v213 offset:2048
	ds_read_b128 v[232:235], v213 offset:4096
	ds_read_b128 v[236:239], v213 offset:6144
	s_and_b64 vcc, exec, s[0:1]
	s_waitcnt lgkmcnt(2)
	v_mfma_f32_16x16x32_f16 v[86:89], v[182:185], v[146:149], v[86:89]
	v_mfma_f32_16x16x32_f16 v[82:85], v[178:181], v[146:149], v[82:85]
	v_mfma_f32_16x16x32_f16 v[90:93], v[178:181], v[150:153], v[90:93]
	v_mfma_f32_16x16x32_f16 v[94:97], v[182:185], v[150:153], v[94:97]
	ds_read_b128 v[240:243], v213 offset:8192
	ds_read_b128 v[244:247], v213 offset:10240
	s_waitcnt lgkmcnt(2)
	v_mfma_f32_16x16x32_f16 v[106:109], v[178:181], v[236:239], v[106:109]
	v_mfma_f32_16x16x32_f16 v[110:113], v[182:185], v[236:239], v[110:113]
	v_mfma_f32_16x16x32_f16 v[98:101], v[178:181], v[232:235], v[98:101]
	v_mfma_f32_16x16x32_f16 v[102:105], v[182:185], v[232:235], v[102:105]
	ds_read_b128 v[232:235], v213 offset:12288
	ds_read_b128 v[236:239], v213 offset:14336
	s_waitcnt lgkmcnt(2)
	v_mfma_f32_16x16x32_f16 v[146:149], v[178:181], v[240:243], v[114:117]
	v_mfma_f32_16x16x32_f16 v[150:153], v[182:185], v[240:243], v[118:121]
	v_mfma_f32_16x16x32_f16 v[154:157], v[178:181], v[244:247], v[122:125]
	v_mfma_f32_16x16x32_f16 v[158:161], v[182:185], v[244:247], v[126:129]
	s_waitcnt lgkmcnt(0)
	v_mfma_f32_16x16x32_f16 v[162:165], v[178:181], v[232:235], v[130:133]
	v_mfma_f32_16x16x32_f16 v[166:169], v[182:185], v[232:235], v[134:137]
	v_mfma_f32_16x16x32_f16 v[170:173], v[178:181], v[236:239], v[138:141]
	v_mfma_f32_16x16x32_f16 v[174:177], v[182:185], v[236:239], v[142:145]
	s_cbranch_vccnz .LBB2_106
	ds_read_b128 v[114:117], v213 offset:16384
	s_waitcnt lgkmcnt(0)
	v_mfma_f32_16x16x32_f16 v[70:73], v[178:181], v[114:117], v[70:73]
	v_mfma_f32_16x16x32_f16 v[78:81], v[182:185], v[114:117], v[78:81]
.LBB2_106:
	v_add_u32_e32 v114, s37, v199
	ds_read_b128 v[178:181], v114
	v_add_u32_e32 v213, s37, v197
	ds_read_b128 v[182:185], v114 offset:2048
	ds_read_b128 v[114:117], v213
	ds_read_b128 v[118:121], v213 offset:2048
	ds_read_b128 v[232:235], v213 offset:4096
	ds_read_b128 v[236:239], v213 offset:6144
	s_and_b64 vcc, exec, s[0:1]
	s_waitcnt lgkmcnt(2)
	v_mfma_f32_16x16x32_f16 v[134:137], v[182:185], v[114:117], v[86:89]
	v_mfma_f32_16x16x32_f16 v[138:141], v[178:181], v[114:117], v[82:85]
	v_mfma_f32_16x16x32_f16 v[130:133], v[178:181], v[118:121], v[90:93]
	v_mfma_f32_16x16x32_f16 v[126:129], v[182:185], v[118:121], v[94:97]
	ds_read_b128 v[240:243], v213 offset:8192
	ds_read_b128 v[244:247], v213 offset:10240
	s_waitcnt lgkmcnt(2)
	v_mfma_f32_16x16x32_f16 v[122:125], v[178:181], v[232:235], v[98:101]
	v_mfma_f32_16x16x32_f16 v[118:121], v[182:185], v[232:235], v[102:105]
	v_mfma_f32_16x16x32_f16 v[114:117], v[178:181], v[236:239], v[106:109]
	v_mfma_f32_16x16x32_f16 v[110:113], v[182:185], v[236:239], v[110:113]
	ds_read_b128 v[232:235], v213 offset:12288
	ds_read_b128 v[236:239], v213 offset:14336
	s_waitcnt lgkmcnt(2)
	v_mfma_f32_16x16x32_f16 v[106:109], v[178:181], v[240:243], v[146:149]
	v_mfma_f32_16x16x32_f16 v[102:105], v[182:185], v[240:243], v[150:153]
	v_mfma_f32_16x16x32_f16 v[98:101], v[178:181], v[244:247], v[154:157]
	v_mfma_f32_16x16x32_f16 v[94:97], v[182:185], v[244:247], v[158:161]
	s_waitcnt lgkmcnt(0)
	v_mfma_f32_16x16x32_f16 v[90:93], v[178:181], v[232:235], v[162:165]
	v_mfma_f32_16x16x32_f16 v[86:89], v[182:185], v[232:235], v[166:169]
	v_mfma_f32_16x16x32_f16 v[142:145], v[178:181], v[236:239], v[170:173]
	v_mfma_f32_16x16x32_f16 v[82:85], v[182:185], v[236:239], v[174:177]
	s_cbranch_vccnz .LBB2_66
	ds_read_b128 v[146:149], v213 offset:16384
	s_waitcnt lgkmcnt(0)
	v_mfma_f32_16x16x32_f16 v[70:73], v[178:181], v[146:149], v[70:73]
	v_mfma_f32_16x16x32_f16 v[78:81], v[182:185], v[146:149], v[78:81]
	s_branch .LBB2_66

.LBB2_114:
	s_setprio 0
	v_and_b32_e32 v0, 16, v0
	v_lshlrev_b32_e32 v1, 2, v191
	s_lshl_b32 s0, s34, 5
	v_add_u32_e32 v70, 12, v1
	v_cmp_eq_u32_e32 vcc, 0, v0
	s_add_i32 s0, s0, s33
	s_mov_b32 s1, 0x3f3504f3
	v_cndmask_b32_e32 v0, v70, v1, vcc
	v_or_b32_e32 v0, s0, v0
	v_ashrrev_i32_e32 v1, 31, v0
	v_lshl_add_u64 v[78:79], v[0:1], 1, s[4:5]
	v_mul_f32_e64 v1, |v74|, s1
	s_mov_b32 s3, 0x3ea7ba05
	v_fma_f32 v0, v1, s3, 1.0
	v_mul_f32_e64 v1, v1, -v1
	v_mul_f32_e32 v1, 0x3fb8aa3b, v1
	v_mul_f32_e64 v71, |v75|, s1
	v_exp_f32_e32 v70, v1
	v_fma_f32 v1, v71, s3, 1.0
	v_rcp_f32_e32 v0, v0
	v_rcp_f32_e32 v1, v1
	s_mov_b32 s8, 0xbfba00e3
	s_mov_b32 s0, 0x3f87dc22
	v_mov_b64_e32 v[80:81], s[8:9]
	v_pk_fma_f32 v[72:73], v[0:1], s[0:1], v[80:81] op_sel_hi:[1,0,0]
	v_mul_f32_e64 v71, v71, -v71
	s_mov_b32 s2, 0x3fb5f0e3
	v_mul_f32_e32 v71, 0x3fb8aa3b, v71
	v_pk_fma_f32 v[72:73], v[72:73], v[0:1], s[2:3] op_sel_hi:[1,1,0]
	s_mov_b32 s4, 0xbe91a98e
	v_exp_f32_e32 v71, v71
	v_pk_fma_f32 v[72:73], v[72:73], v[0:1], s[4:5] op_sel_hi:[1,1,0]
	s_mov_b32 s6, 0x3e827906
	v_pk_fma_f32 v[72:73], v[72:73], v[0:1], s[6:7] op_sel_hi:[1,1,0]
	v_cmp_le_f32_e32 vcc, 0, v75
	v_pk_mul_f32 v[0:1], v[0:1], v[72:73]
	s_nop 0
	v_pk_mul_f32 v[0:1], v[0:1], 0.5 op_sel_hi:[1,0]
	s_nop 0
	v_pk_mul_f32 v[72:73], v[70:71], v[0:1]
	v_pk_fma_f32 v[0:1], v[70:71], v[0:1], 1.0 op_sel_hi:[1,1,0] neg_lo:[1,0,0] neg_hi:[1,0,0]
	v_mul_f32_e64 v71, |v76|, s1
	v_cndmask_b32_e32 v1, v73, v1, vcc
	v_cmp_le_f32_e32 vcc, 0, v74
	v_mul_f32_e64 v73, |v77|, s1
	s_nop 0
	v_cndmask_b32_e32 v0, v72, v0, vcc
	v_pk_mul_f32 v[0:1], v[74:75], v[0:1]
	v_cmp_le_f32_e32 vcc, 0, v77
	s_waitcnt vmcnt(0)
	v_pk_mul_f32 v[0:1], v[220:221], v[0:1] op_sel_hi:[0,1]
	v_cvt_pk_f16_f32 v70, v0, v1
	v_fma_f32 v0, v71, s3, 1.0
	v_fma_f32 v1, v73, s3, 1.0
	v_rcp_f32_e32 v0, v0
	v_rcp_f32_e32 v1, v1
	v_mul_f32_e64 v71, v71, -v71
	v_mul_f32_e32 v71, 0x3fb8aa3b, v71
	v_exp_f32_e32 v72, v71
	v_pk_fma_f32 v[74:75], v[0:1], s[0:1], v[80:81] op_sel_hi:[1,0,0]
	v_mul_f32_e64 v71, v73, -v73
	v_mul_f32_e32 v71, 0x3fb8aa3b, v71
	v_pk_fma_f32 v[74:75], v[74:75], v[0:1], s[2:3] op_sel_hi:[1,1,0]
	v_exp_f32_e32 v73, v71
	v_pk_fma_f32 v[74:75], v[74:75], v[0:1], s[4:5] op_sel_hi:[1,1,0]
	s_nop 0
	v_pk_fma_f32 v[74:75], v[74:75], v[0:1], s[6:7] op_sel_hi:[1,1,0]
	s_nop 0
	v_pk_mul_f32 v[0:1], v[0:1], v[74:75]
	s_nop 0
	v_pk_mul_f32 v[0:1], v[0:1], 0.5 op_sel_hi:[1,0]
	s_nop 0
	v_pk_mul_f32 v[74:75], v[72:73], v[0:1]
	v_pk_fma_f32 v[0:1], v[72:73], v[0:1], 1.0 op_sel_hi:[1,1,0] neg_lo:[1,0,0] neg_hi:[1,0,0]
	v_mul_f32_e64 v72, |v66|, s1
	v_cndmask_b32_e32 v1, v75, v1, vcc
	v_cmp_le_f32_e32 vcc, 0, v76
	v_mul_f32_e64 v73, |v67|, s1
	s_nop 0
	v_cndmask_b32_e32 v0, v74, v0, vcc
	v_pk_mul_f32 v[0:1], v[76:77], v[0:1]
	v_cmp_le_f32_e32 vcc, 0, v67
	v_pk_mul_f32 v[0:1], v[220:221], v[0:1] op_sel_hi:[0,1]
	v_cvt_pk_f16_f32 v71, v0, v1
	v_fma_f32 v0, v72, s3, 1.0
	v_fma_f32 v1, v73, s3, 1.0
	v_rcp_f32_e32 v0, v0
	v_rcp_f32_e32 v1, v1
	v_mul_f32_e64 v72, v72, -v72
	v_mul_f32_e64 v73, v73, -v73
	v_mul_f32_e32 v72, 0x3fb8aa3b, v72
	v_pk_fma_f32 v[74:75], v[0:1], s[0:1], v[80:81] op_sel_hi:[1,0,0]
	v_mul_f32_e32 v73, 0x3fb8aa3b, v73
	v_pk_fma_f32 v[74:75], v[74:75], v[0:1], s[2:3] op_sel_hi:[1,1,0]
	v_exp_f32_e32 v72, v72
	v_exp_f32_e32 v73, v73
	v_pk_fma_f32 v[74:75], v[74:75], v[0:1], s[4:5] op_sel_hi:[1,1,0]
	s_nop 0
	v_pk_fma_f32 v[74:75], v[74:75], v[0:1], s[6:7] op_sel_hi:[1,1,0]
	s_nop 0
	v_pk_mul_f32 v[0:1], v[0:1], v[74:75]
	s_nop 0
	v_pk_mul_f32 v[0:1], v[0:1], 0.5 op_sel_hi:[1,0]
	s_nop 0
	v_pk_mul_f32 v[74:75], v[72:73], v[0:1]
	v_pk_fma_f32 v[0:1], v[72:73], v[0:1], 1.0 op_sel_hi:[1,1,0] neg_lo:[1,0,0] neg_hi:[1,0,0]
	s_nop 0
	v_cndmask_b32_e32 v1, v75, v1, vcc
	v_cmp_le_f32_e32 vcc, 0, v66
	s_nop 1
	v_cndmask_b32_e32 v0, v74, v0, vcc
	v_pk_mul_f32 v[0:1], v[66:67], v[0:1]
	v_mul_f32_e64 v66, |v68|, s1
	v_pk_mul_f32 v[0:1], v[220:221], v[0:1] op_sel_hi:[0,1]
	v_mul_f32_e64 v67, |v69|, s1
	v_cvt_pk_f16_f32 v72, v0, v1
	v_fma_f32 v0, v66, s3, 1.0
	v_fma_f32 v1, v67, s3, 1.0
	v_rcp_f32_e32 v0, v0
	v_rcp_f32_e32 v1, v1
	v_mul_f32_e64 v66, v66, -v66
	v_mul_f32_e64 v67, v67, -v67
	v_mul_f32_e32 v66, 0x3fb8aa3b, v66
	v_pk_fma_f32 v[74:75], v[0:1], s[0:1], v[80:81] op_sel_hi:[1,0,0]
	v_mul_f32_e32 v67, 0x3fb8aa3b, v67
	v_pk_fma_f32 v[74:75], v[74:75], v[0:1], s[2:3] op_sel_hi:[1,1,0]
	v_exp_f32_e32 v66, v66
	v_exp_f32_e32 v67, v67
	v_pk_fma_f32 v[74:75], v[74:75], v[0:1], s[4:5] op_sel_hi:[1,1,0]
	v_cmp_le_f32_e32 vcc, 0, v69
	v_pk_fma_f32 v[74:75], v[74:75], v[0:1], s[6:7] op_sel_hi:[1,1,0]
	v_permlane16_swap_b32_e32 v70, v72
	v_pk_mul_f32 v[0:1], v[0:1], v[74:75]
	s_nop 0
	v_pk_mul_f32 v[0:1], v[0:1], 0.5 op_sel_hi:[1,0]
	s_nop 0
	v_pk_mul_f32 v[74:75], v[66:67], v[0:1]
	v_pk_fma_f32 v[0:1], v[66:67], v[0:1], 1.0 op_sel_hi:[1,1,0] neg_lo:[1,0,0] neg_hi:[1,0,0]
	s_nop 0
	v_cndmask_b32_e32 v1, v75, v1, vcc
	v_cmp_le_f32_e32 vcc, 0, v68
	s_nop 1
	v_cndmask_b32_e32 v0, v74, v0, vcc
	v_pk_mul_f32 v[0:1], v[68:69], v[0:1]
	v_cmp_lt_i32_e32 vcc, -1, v218
	v_pk_mul_f32 v[0:1], v[220:221], v[0:1] op_sel_hi:[0,1]
	v_cvt_pk_f16_f32 v73, v0, v1
	s_nop 1
	v_permlane16_swap_b32_e32 v71, v73
	s_and_saveexec_b64 s[10:11], vcc
	s_cbranch_execz .LBB2_116
	v_mov_b32_e32 v219, 0
	v_lshlrev_b64 v[0:1], 10, v[218:219]
	v_lshl_add_u64 v[0:1], v[78:79], 0, v[0:1]
	global_store_dwordx4 v[0:1], v[70:73], off sc1
.LBB2_116:
	s_or_b64 exec, exec, s[10:11]
	v_mul_f32_e64 v1, |v62|, s1
	v_mul_f32_e64 v67, |v63|, s1
	v_fma_f32 v0, v1, s3, 1.0
	v_mul_f32_e64 v66, v1, -v1
	v_fma_f32 v1, v67, s3, 1.0
	v_rcp_f32_e32 v0, v0
	v_rcp_f32_e32 v1, v1
	v_mov_b64_e32 v[68:69], s[8:9]
	v_mul_f32_e64 v67, v67, -v67
	v_mul_f32_e32 v66, 0x3fb8aa3b, v66
	v_pk_fma_f32 v[70:71], v[0:1], s[0:1], v[68:69] op_sel_hi:[1,0,0]
	v_mul_f32_e32 v67, 0x3fb8aa3b, v67
	v_pk_fma_f32 v[70:71], v[70:71], v[0:1], s[2:3] op_sel_hi:[1,1,0]
	v_exp_f32_e32 v66, v66
	v_exp_f32_e32 v67, v67
	v_pk_fma_f32 v[70:71], v[70:71], v[0:1], s[4:5] op_sel_hi:[1,1,0]
	v_cmp_le_f32_e32 vcc, 0, v63
	v_pk_fma_f32 v[70:71], v[70:71], v[0:1], s[6:7] op_sel_hi:[1,1,0]
	s_nop 0
	v_pk_mul_f32 v[0:1], v[0:1], v[70:71]
	s_nop 0
	v_pk_mul_f32 v[0:1], v[0:1], 0.5 op_sel_hi:[1,0]
	s_nop 0
	v_pk_mul_f32 v[70:71], v[66:67], v[0:1]
	v_pk_fma_f32 v[0:1], v[66:67], v[0:1], 1.0 op_sel_hi:[1,1,0] neg_lo:[1,0,0] neg_hi:[1,0,0]
	v_mul_f32_e64 v67, |v65|, s1
	v_cndmask_b32_e32 v1, v71, v1, vcc
	v_cmp_le_f32_e32 vcc, 0, v62
	s_nop 1
	v_cndmask_b32_e32 v0, v70, v0, vcc
	v_pk_mul_f32 v[0:1], v[62:63], v[0:1]
	v_mul_f32_e64 v63, |v64|, s1
	v_pk_mul_f32 v[0:1], v[216:217], v[0:1] op_sel_hi:[0,1]
	v_cvt_pk_f16_f32 v62, v0, v1
	v_fma_f32 v0, v63, s3, 1.0
	v_fma_f32 v1, v67, s3, 1.0
	v_rcp_f32_e32 v0, v0
	v_rcp_f32_e32 v1, v1
	v_mul_f32_e64 v63, v63, -v63
	v_mul_f32_e32 v63, 0x3fb8aa3b, v63
	v_exp_f32_e32 v66, v63
	v_pk_fma_f32 v[70:71], v[0:1], s[0:1], v[68:69] op_sel_hi:[1,0,0]
	v_mul_f32_e64 v63, v67, -v67
	v_mul_f32_e32 v63, 0x3fb8aa3b, v63
	v_pk_fma_f32 v[70:71], v[70:71], v[0:1], s[2:3] op_sel_hi:[1,1,0]
	v_exp_f32_e32 v67, v63
	v_pk_fma_f32 v[70:71], v[70:71], v[0:1], s[4:5] op_sel_hi:[1,1,0]
	v_cmp_le_f32_e32 vcc, 0, v65
	v_pk_fma_f32 v[70:71], v[70:71], v[0:1], s[6:7] op_sel_hi:[1,1,0]
	s_nop 0
	v_pk_mul_f32 v[0:1], v[0:1], v[70:71]
	s_nop 0
	v_pk_mul_f32 v[0:1], v[0:1], 0.5 op_sel_hi:[1,0]
	s_nop 0
	v_pk_mul_f32 v[70:71], v[66:67], v[0:1]
	v_pk_fma_f32 v[0:1], v[66:67], v[0:1], 1.0 op_sel_hi:[1,1,0] neg_lo:[1,0,0] neg_hi:[1,0,0]
	s_nop 0
	v_cndmask_b32_e32 v1, v71, v1, vcc
	v_cmp_le_f32_e32 vcc, 0, v64
	s_nop 1
	v_cndmask_b32_e32 v0, v70, v0, vcc
	v_pk_mul_f32 v[0:1], v[64:65], v[0:1]
	v_mul_f32_e64 v64, |v58|, s1
	v_pk_mul_f32 v[0:1], v[216:217], v[0:1] op_sel_hi:[0,1]
	v_mul_f32_e64 v65, |v59|, s1
	v_cvt_pk_f16_f32 v63, v0, v1
	v_fma_f32 v0, v64, s3, 1.0
	v_fma_f32 v1, v65, s3, 1.0
	v_rcp_f32_e32 v0, v0
	v_rcp_f32_e32 v1, v1
	v_mul_f32_e64 v64, v64, -v64
	v_mul_f32_e64 v65, v65, -v65
	v_mul_f32_e32 v64, 0x3fb8aa3b, v64
	v_pk_fma_f32 v[66:67], v[0:1], s[0:1], v[68:69] op_sel_hi:[1,0,0]
	v_mul_f32_e32 v65, 0x3fb8aa3b, v65
	v_pk_fma_f32 v[66:67], v[66:67], v[0:1], s[2:3] op_sel_hi:[1,1,0]
	v_exp_f32_e32 v64, v64
	v_exp_f32_e32 v65, v65
	v_pk_fma_f32 v[66:67], v[66:67], v[0:1], s[4:5] op_sel_hi:[1,1,0]
	v_cmp_le_f32_e32 vcc, 0, v59
	v_pk_fma_f32 v[66:67], v[66:67], v[0:1], s[6:7] op_sel_hi:[1,1,0]
	s_nop 0
	v_pk_mul_f32 v[0:1], v[0:1], v[66:67]
	s_nop 0
	v_pk_mul_f32 v[0:1], v[0:1], 0.5 op_sel_hi:[1,0]
	s_nop 0
	v_pk_mul_f32 v[66:67], v[64:65], v[0:1]
	v_pk_fma_f32 v[0:1], v[64:65], v[0:1], 1.0 op_sel_hi:[1,1,0] neg_lo:[1,0,0] neg_hi:[1,0,0]
	s_nop 0
	v_cndmask_b32_e32 v1, v67, v1, vcc
	v_cmp_le_f32_e32 vcc, 0, v58
	s_nop 1
	v_cndmask_b32_e32 v0, v66, v0, vcc
	v_pk_mul_f32 v[0:1], v[58:59], v[0:1]
	v_mul_f32_e64 v58, |v60|, s1
	v_pk_mul_f32 v[0:1], v[216:217], v[0:1] op_sel_hi:[0,1]
	v_mul_f32_e64 v59, |v61|, s1
	v_cvt_pk_f16_f32 v64, v0, v1
	v_fma_f32 v0, v58, s3, 1.0
	v_fma_f32 v1, v59, s3, 1.0
	v_rcp_f32_e32 v0, v0
	v_rcp_f32_e32 v1, v1
	v_mul_f32_e64 v58, v58, -v58
	v_mul_f32_e64 v59, v59, -v59
	v_mul_f32_e32 v58, 0x3fb8aa3b, v58
	v_pk_fma_f32 v[66:67], v[0:1], s[0:1], v[68:69] op_sel_hi:[1,0,0]
	v_mul_f32_e32 v59, 0x3fb8aa3b, v59
	v_pk_fma_f32 v[66:67], v[66:67], v[0:1], s[2:3] op_sel_hi:[1,1,0]
	v_exp_f32_e32 v58, v58
	v_exp_f32_e32 v59, v59
	v_pk_fma_f32 v[66:67], v[66:67], v[0:1], s[4:5] op_sel_hi:[1,1,0]
	v_cmp_le_f32_e32 vcc, 0, v61
	v_pk_fma_f32 v[66:67], v[66:67], v[0:1], s[6:7] op_sel_hi:[1,1,0]
	v_permlane16_swap_b32_e32 v62, v64
	v_pk_mul_f32 v[0:1], v[0:1], v[66:67]
	s_nop 0
	v_pk_mul_f32 v[0:1], v[0:1], 0.5 op_sel_hi:[1,0]
	s_nop 0
	v_pk_mul_f32 v[66:67], v[58:59], v[0:1]
	v_pk_fma_f32 v[0:1], v[58:59], v[0:1], 1.0 op_sel_hi:[1,1,0] neg_lo:[1,0,0] neg_hi:[1,0,0]
	s_nop 0
	v_cndmask_b32_e32 v1, v67, v1, vcc
	v_cmp_le_f32_e32 vcc, 0, v60
	s_nop 1
	v_cndmask_b32_e32 v0, v66, v0, vcc
	v_pk_mul_f32 v[0:1], v[60:61], v[0:1]
	v_cmp_lt_i32_e32 vcc, -1, v214
	v_pk_mul_f32 v[0:1], v[216:217], v[0:1] op_sel_hi:[0,1]
	v_cvt_pk_f16_f32 v65, v0, v1
	s_nop 1
	v_permlane16_swap_b32_e32 v63, v65
	s_and_saveexec_b64 s[0:1], vcc
	s_cbranch_execz .LBB2_118
	v_mov_b32_e32 v215, 0
	v_lshlrev_b64 v[0:1], 10, v[214:215]
	v_lshl_add_u64 v[0:1], v[78:79], 0, v[0:1]
	global_store_dwordx4 v[0:1], v[62:65], off sc1
.LBB2_118:
	s_or_b64 exec, exec, s[0:1]
	s_mov_b32 s1, 0x3f3504f3
	v_mul_f32_e64 v1, |v54|, s1
	v_fma_f32 v0, v1, s3, 1.0
	v_mul_f32_e64 v1, v1, -v1
	v_mul_f32_e32 v1, 0x3fb8aa3b, v1
	v_mul_f32_e64 v59, |v55|, s1
	v_exp_f32_e32 v58, v1
	v_fma_f32 v1, v59, s3, 1.0
	v_rcp_f32_e32 v0, v0
	v_rcp_f32_e32 v1, v1
	s_mov_b32 s0, 0x3f87dc22
	v_mov_b64_e32 v[60:61], s[8:9]
	v_mul_f32_e64 v59, v59, -v59
	v_pk_fma_f32 v[62:63], v[0:1], s[0:1], v[60:61] op_sel_hi:[1,0,0]
	v_mul_f32_e32 v59, 0x3fb8aa3b, v59
	v_pk_fma_f32 v[62:63], v[62:63], v[0:1], s[2:3] op_sel_hi:[1,1,0]
	v_exp_f32_e32 v59, v59
	v_pk_fma_f32 v[62:63], v[62:63], v[0:1], s[4:5] op_sel_hi:[1,1,0]
	v_cmp_le_f32_e32 vcc, 0, v55
	v_pk_fma_f32 v[62:63], v[62:63], v[0:1], s[6:7] op_sel_hi:[1,1,0]
	s_nop 0
	v_pk_mul_f32 v[0:1], v[0:1], v[62:63]
	s_nop 0
	v_pk_mul_f32 v[0:1], v[0:1], 0.5 op_sel_hi:[1,0]
	s_nop 0
	v_pk_mul_f32 v[62:63], v[58:59], v[0:1]
	v_pk_fma_f32 v[0:1], v[58:59], v[0:1], 1.0 op_sel_hi:[1,1,0] neg_lo:[1,0,0] neg_hi:[1,0,0]
	v_mul_f32_e64 v59, |v57|, s1
	v_cndmask_b32_e32 v1, v63, v1, vcc
	v_cmp_le_f32_e32 vcc, 0, v54
	s_nop 1
	v_cndmask_b32_e32 v0, v62, v0, vcc
	v_pk_mul_f32 v[0:1], v[54:55], v[0:1]
	v_mul_f32_e64 v55, |v56|, s1
	v_pk_mul_f32 v[0:1], v[212:213], v[0:1] op_sel_hi:[0,1]
	v_cvt_pk_f16_f32 v54, v0, v1
	v_fma_f32 v0, v55, s3, 1.0
	v_fma_f32 v1, v59, s3, 1.0
	v_rcp_f32_e32 v0, v0
	v_rcp_f32_e32 v1, v1
	v_mul_f32_e64 v55, v55, -v55
	v_mul_f32_e32 v55, 0x3fb8aa3b, v55
	v_exp_f32_e32 v58, v55
	v_pk_fma_f32 v[62:63], v[0:1], s[0:1], v[60:61] op_sel_hi:[1,0,0]
	v_mul_f32_e64 v55, v59, -v59
	v_mul_f32_e32 v55, 0x3fb8aa3b, v55
	v_pk_fma_f32 v[62:63], v[62:63], v[0:1], s[2:3] op_sel_hi:[1,1,0]
	v_exp_f32_e32 v59, v55
	v_pk_fma_f32 v[62:63], v[62:63], v[0:1], s[4:5] op_sel_hi:[1,1,0]
	v_cmp_le_f32_e32 vcc, 0, v57
	v_pk_fma_f32 v[62:63], v[62:63], v[0:1], s[6:7] op_sel_hi:[1,1,0]
	s_nop 0
	v_pk_mul_f32 v[0:1], v[0:1], v[62:63]
	s_nop 0
	v_pk_mul_f32 v[0:1], v[0:1], 0.5 op_sel_hi:[1,0]
	s_nop 0
	v_pk_mul_f32 v[62:63], v[58:59], v[0:1]
	v_pk_fma_f32 v[0:1], v[58:59], v[0:1], 1.0 op_sel_hi:[1,1,0] neg_lo:[1,0,0] neg_hi:[1,0,0]
	s_nop 0
	v_cndmask_b32_e32 v1, v63, v1, vcc
	v_cmp_le_f32_e32 vcc, 0, v56
	s_nop 1
	v_cndmask_b32_e32 v0, v62, v0, vcc
	v_pk_mul_f32 v[0:1], v[56:57], v[0:1]
	v_mul_f32_e64 v56, |v50|, s1
	v_pk_mul_f32 v[0:1], v[212:213], v[0:1] op_sel_hi:[0,1]
	v_mul_f32_e64 v57, |v51|, s1
	v_cvt_pk_f16_f32 v55, v0, v1
	v_fma_f32 v0, v56, s3, 1.0
	v_fma_f32 v1, v57, s3, 1.0
	v_rcp_f32_e32 v0, v0
	v_rcp_f32_e32 v1, v1
	v_mul_f32_e64 v56, v56, -v56
	v_mul_f32_e64 v57, v57, -v57
	v_mul_f32_e32 v56, 0x3fb8aa3b, v56
	v_pk_fma_f32 v[58:59], v[0:1], s[0:1], v[60:61] op_sel_hi:[1,0,0]
	v_mul_f32_e32 v57, 0x3fb8aa3b, v57
	v_pk_fma_f32 v[58:59], v[58:59], v[0:1], s[2:3] op_sel_hi:[1,1,0]
	v_exp_f32_e32 v56, v56
	v_exp_f32_e32 v57, v57
	v_pk_fma_f32 v[58:59], v[58:59], v[0:1], s[4:5] op_sel_hi:[1,1,0]
	v_cmp_le_f32_e32 vcc, 0, v51
	v_pk_fma_f32 v[58:59], v[58:59], v[0:1], s[6:7] op_sel_hi:[1,1,0]
	s_nop 0
	v_pk_mul_f32 v[0:1], v[0:1], v[58:59]
	s_nop 0
	v_pk_mul_f32 v[0:1], v[0:1], 0.5 op_sel_hi:[1,0]
	s_nop 0
	v_pk_mul_f32 v[58:59], v[56:57], v[0:1]
	v_pk_fma_f32 v[0:1], v[56:57], v[0:1], 1.0 op_sel_hi:[1,1,0] neg_lo:[1,0,0] neg_hi:[1,0,0]
	s_nop 0
	v_cndmask_b32_e32 v1, v59, v1, vcc
	v_cmp_le_f32_e32 vcc, 0, v50
	s_nop 1
	v_cndmask_b32_e32 v0, v58, v0, vcc
	v_pk_mul_f32 v[0:1], v[50:51], v[0:1]
	v_mul_f32_e64 v50, |v52|, s1
	v_pk_mul_f32 v[0:1], v[212:213], v[0:1] op_sel_hi:[0,1]
	v_mul_f32_e64 v51, |v53|, s1
	v_cvt_pk_f16_f32 v56, v0, v1
	v_fma_f32 v0, v50, s3, 1.0
	v_fma_f32 v1, v51, s3, 1.0
	v_rcp_f32_e32 v0, v0
	v_rcp_f32_e32 v1, v1
	v_mul_f32_e64 v50, v50, -v50
	v_mul_f32_e64 v51, v51, -v51
	v_mul_f32_e32 v50, 0x3fb8aa3b, v50
	v_pk_fma_f32 v[58:59], v[0:1], s[0:1], v[60:61] op_sel_hi:[1,0,0]
	v_mul_f32_e32 v51, 0x3fb8aa3b, v51
	v_pk_fma_f32 v[58:59], v[58:59], v[0:1], s[2:3] op_sel_hi:[1,1,0]
	v_exp_f32_e32 v50, v50
	v_exp_f32_e32 v51, v51
	v_pk_fma_f32 v[58:59], v[58:59], v[0:1], s[4:5] op_sel_hi:[1,1,0]
	v_cmp_le_f32_e32 vcc, 0, v53
	v_pk_fma_f32 v[58:59], v[58:59], v[0:1], s[6:7] op_sel_hi:[1,1,0]
	v_permlane16_swap_b32_e32 v54, v56
	v_pk_mul_f32 v[0:1], v[0:1], v[58:59]
	s_nop 0
	v_pk_mul_f32 v[0:1], v[0:1], 0.5 op_sel_hi:[1,0]
	s_nop 0
	v_pk_mul_f32 v[58:59], v[50:51], v[0:1]
	v_pk_fma_f32 v[0:1], v[50:51], v[0:1], 1.0 op_sel_hi:[1,1,0] neg_lo:[1,0,0] neg_hi:[1,0,0]
	s_nop 0
	v_cndmask_b32_e32 v1, v59, v1, vcc
	v_cmp_le_f32_e32 vcc, 0, v52
	s_nop 1
	v_cndmask_b32_e32 v0, v58, v0, vcc
	v_pk_mul_f32 v[0:1], v[52:53], v[0:1]
	v_cmp_lt_i32_e32 vcc, -1, v210
	v_pk_mul_f32 v[0:1], v[212:213], v[0:1] op_sel_hi:[0,1]
	v_cvt_pk_f16_f32 v57, v0, v1
	s_nop 1
	v_permlane16_swap_b32_e32 v55, v57
	s_and_saveexec_b64 s[10:11], vcc
	s_cbranch_execz .LBB2_120
	v_mov_b32_e32 v211, 0
	v_lshlrev_b64 v[0:1], 10, v[210:211]
	v_lshl_add_u64 v[0:1], v[78:79], 0, v[0:1]
	global_store_dwordx4 v[0:1], v[54:57], off sc1
.LBB2_120:
	s_or_b64 exec, exec, s[10:11]
	v_mul_f32_e64 v1, |v46|, s1
	v_mul_f32_e64 v51, |v47|, s1
	v_fma_f32 v0, v1, s3, 1.0
	v_mul_f32_e64 v50, v1, -v1
	v_fma_f32 v1, v51, s3, 1.0
	v_rcp_f32_e32 v0, v0
	v_rcp_f32_e32 v1, v1
	v_mov_b64_e32 v[52:53], s[8:9]
	v_mul_f32_e64 v51, v51, -v51
	v_mul_f32_e32 v50, 0x3fb8aa3b, v50
	v_pk_fma_f32 v[54:55], v[0:1], s[0:1], v[52:53] op_sel_hi:[1,0,0]
	v_mul_f32_e32 v51, 0x3fb8aa3b, v51
	v_pk_fma_f32 v[54:55], v[54:55], v[0:1], s[2:3] op_sel_hi:[1,1,0]
	v_exp_f32_e32 v50, v50
	v_exp_f32_e32 v51, v51
	v_pk_fma_f32 v[54:55], v[54:55], v[0:1], s[4:5] op_sel_hi:[1,1,0]
	v_cmp_le_f32_e32 vcc, 0, v47
	v_pk_fma_f32 v[54:55], v[54:55], v[0:1], s[6:7] op_sel_hi:[1,1,0]
	s_nop 0
	v_pk_mul_f32 v[0:1], v[0:1], v[54:55]
	s_nop 0
	v_pk_mul_f32 v[0:1], v[0:1], 0.5 op_sel_hi:[1,0]
	s_nop 0
	v_pk_mul_f32 v[54:55], v[50:51], v[0:1]
	v_pk_fma_f32 v[0:1], v[50:51], v[0:1], 1.0 op_sel_hi:[1,1,0] neg_lo:[1,0,0] neg_hi:[1,0,0]
	v_mul_f32_e64 v51, |v49|, s1
	v_cndmask_b32_e32 v1, v55, v1, vcc
	v_cmp_le_f32_e32 vcc, 0, v46
	s_nop 1
	v_cndmask_b32_e32 v0, v54, v0, vcc
	v_pk_mul_f32 v[0:1], v[46:47], v[0:1]
	v_mul_f32_e64 v47, |v48|, s1
	v_pk_mul_f32 v[0:1], v[208:209], v[0:1] op_sel_hi:[0,1]
	v_cvt_pk_f16_f32 v46, v0, v1
	v_fma_f32 v0, v47, s3, 1.0
	v_fma_f32 v1, v51, s3, 1.0
	v_rcp_f32_e32 v0, v0
	v_rcp_f32_e32 v1, v1
	v_mul_f32_e64 v47, v47, -v47
	v_mul_f32_e32 v47, 0x3fb8aa3b, v47
	v_exp_f32_e32 v50, v47
	v_pk_fma_f32 v[54:55], v[0:1], s[0:1], v[52:53] op_sel_hi:[1,0,0]
	v_mul_f32_e64 v47, v51, -v51
	v_mul_f32_e32 v47, 0x3fb8aa3b, v47
	v_pk_fma_f32 v[54:55], v[54:55], v[0:1], s[2:3] op_sel_hi:[1,1,0]
	v_exp_f32_e32 v51, v47
	v_pk_fma_f32 v[54:55], v[54:55], v[0:1], s[4:5] op_sel_hi:[1,1,0]
	v_cmp_le_f32_e32 vcc, 0, v49
	v_pk_fma_f32 v[54:55], v[54:55], v[0:1], s[6:7] op_sel_hi:[1,1,0]
	s_nop 0
	v_pk_mul_f32 v[0:1], v[0:1], v[54:55]
	s_nop 0
	v_pk_mul_f32 v[0:1], v[0:1], 0.5 op_sel_hi:[1,0]
	s_nop 0
	v_pk_mul_f32 v[54:55], v[50:51], v[0:1]
	v_pk_fma_f32 v[0:1], v[50:51], v[0:1], 1.0 op_sel_hi:[1,1,0] neg_lo:[1,0,0] neg_hi:[1,0,0]
	s_nop 0
	v_cndmask_b32_e32 v1, v55, v1, vcc
	v_cmp_le_f32_e32 vcc, 0, v48
	s_nop 1
	v_cndmask_b32_e32 v0, v54, v0, vcc
	v_pk_mul_f32 v[0:1], v[48:49], v[0:1]
	v_mul_f32_e64 v48, |v42|, s1
	v_pk_mul_f32 v[0:1], v[208:209], v[0:1] op_sel_hi:[0,1]
	v_mul_f32_e64 v49, |v43|, s1
	v_cvt_pk_f16_f32 v47, v0, v1
	v_fma_f32 v0, v48, s3, 1.0
	v_fma_f32 v1, v49, s3, 1.0
	v_rcp_f32_e32 v0, v0
	v_rcp_f32_e32 v1, v1
	v_mul_f32_e64 v48, v48, -v48
	v_mul_f32_e64 v49, v49, -v49
	v_mul_f32_e32 v48, 0x3fb8aa3b, v48
	v_pk_fma_f32 v[50:51], v[0:1], s[0:1], v[52:53] op_sel_hi:[1,0,0]
	v_mul_f32_e32 v49, 0x3fb8aa3b, v49
	v_pk_fma_f32 v[50:51], v[50:51], v[0:1], s[2:3] op_sel_hi:[1,1,0]
	v_exp_f32_e32 v48, v48
	v_exp_f32_e32 v49, v49
	v_pk_fma_f32 v[50:51], v[50:51], v[0:1], s[4:5] op_sel_hi:[1,1,0]
	v_cmp_le_f32_e32 vcc, 0, v43
	v_pk_fma_f32 v[50:51], v[50:51], v[0:1], s[6:7] op_sel_hi:[1,1,0]
	s_nop 0
	v_pk_mul_f32 v[0:1], v[0:1], v[50:51]
	s_nop 0
	v_pk_mul_f32 v[0:1], v[0:1], 0.5 op_sel_hi:[1,0]
	s_nop 0
	v_pk_mul_f32 v[50:51], v[48:49], v[0:1]
	v_pk_fma_f32 v[0:1], v[48:49], v[0:1], 1.0 op_sel_hi:[1,1,0] neg_lo:[1,0,0] neg_hi:[1,0,0]
	s_nop 0
	v_cndmask_b32_e32 v1, v51, v1, vcc
	v_cmp_le_f32_e32 vcc, 0, v42
	s_nop 1
	v_cndmask_b32_e32 v0, v50, v0, vcc
	v_pk_mul_f32 v[0:1], v[42:43], v[0:1]
	v_mul_f32_e64 v42, |v44|, s1
	v_pk_mul_f32 v[0:1], v[208:209], v[0:1] op_sel_hi:[0,1]
	v_mul_f32_e64 v43, |v45|, s1
	v_cvt_pk_f16_f32 v48, v0, v1
	v_fma_f32 v0, v42, s3, 1.0
	v_fma_f32 v1, v43, s3, 1.0
	v_rcp_f32_e32 v0, v0
	v_rcp_f32_e32 v1, v1
	v_mul_f32_e64 v42, v42, -v42
	v_mul_f32_e64 v43, v43, -v43
	v_mul_f32_e32 v42, 0x3fb8aa3b, v42
	v_pk_fma_f32 v[50:51], v[0:1], s[0:1], v[52:53] op_sel_hi:[1,0,0]
	v_mul_f32_e32 v43, 0x3fb8aa3b, v43
	v_pk_fma_f32 v[50:51], v[50:51], v[0:1], s[2:3] op_sel_hi:[1,1,0]
	v_exp_f32_e32 v42, v42
	v_exp_f32_e32 v43, v43
	v_pk_fma_f32 v[50:51], v[50:51], v[0:1], s[4:5] op_sel_hi:[1,1,0]
	v_cmp_le_f32_e32 vcc, 0, v45
	v_pk_fma_f32 v[50:51], v[50:51], v[0:1], s[6:7] op_sel_hi:[1,1,0]
	v_permlane16_swap_b32_e32 v46, v48
	v_pk_mul_f32 v[0:1], v[0:1], v[50:51]
	s_nop 0
	v_pk_mul_f32 v[0:1], v[0:1], 0.5 op_sel_hi:[1,0]
	s_nop 0
	v_pk_mul_f32 v[50:51], v[42:43], v[0:1]
	v_pk_fma_f32 v[0:1], v[42:43], v[0:1], 1.0 op_sel_hi:[1,1,0] neg_lo:[1,0,0] neg_hi:[1,0,0]
	s_nop 0
	v_cndmask_b32_e32 v1, v51, v1, vcc
	v_cmp_le_f32_e32 vcc, 0, v44
	s_nop 1
	v_cndmask_b32_e32 v0, v50, v0, vcc
	v_pk_mul_f32 v[0:1], v[44:45], v[0:1]
	v_cmp_lt_i32_e32 vcc, -1, v206
	v_pk_mul_f32 v[0:1], v[208:209], v[0:1] op_sel_hi:[0,1]
	v_cvt_pk_f16_f32 v49, v0, v1
	s_nop 1
	v_permlane16_swap_b32_e32 v47, v49
	s_and_saveexec_b64 s[0:1], vcc
	s_cbranch_execz .LBB2_122
	v_mov_b32_e32 v207, 0
	v_lshlrev_b64 v[0:1], 10, v[206:207]
	v_lshl_add_u64 v[0:1], v[78:79], 0, v[0:1]
	global_store_dwordx4 v[0:1], v[46:49], off sc1
.LBB2_122:
	s_or_b64 exec, exec, s[0:1]
	s_mov_b32 s1, 0x3f3504f3
	v_mul_f32_e64 v1, |v38|, s1
	v_fma_f32 v0, v1, s3, 1.0
	v_mul_f32_e64 v1, v1, -v1
	v_mul_f32_e32 v1, 0x3fb8aa3b, v1
	v_mul_f32_e64 v43, |v39|, s1
	v_exp_f32_e32 v42, v1
	v_fma_f32 v1, v43, s3, 1.0
	v_rcp_f32_e32 v0, v0
	v_rcp_f32_e32 v1, v1
	s_mov_b32 s0, 0x3f87dc22
	v_mov_b64_e32 v[44:45], s[8:9]
	v_mul_f32_e64 v43, v43, -v43
	v_pk_fma_f32 v[46:47], v[0:1], s[0:1], v[44:45] op_sel_hi:[1,0,0]
	v_mul_f32_e32 v43, 0x3fb8aa3b, v43
	v_pk_fma_f32 v[46:47], v[46:47], v[0:1], s[2:3] op_sel_hi:[1,1,0]
	v_exp_f32_e32 v43, v43
	v_pk_fma_f32 v[46:47], v[46:47], v[0:1], s[4:5] op_sel_hi:[1,1,0]
	v_cmp_le_f32_e32 vcc, 0, v39
	v_pk_fma_f32 v[46:47], v[46:47], v[0:1], s[6:7] op_sel_hi:[1,1,0]
	s_nop 0
	v_pk_mul_f32 v[0:1], v[0:1], v[46:47]
	s_nop 0
	v_pk_mul_f32 v[0:1], v[0:1], 0.5 op_sel_hi:[1,0]
	s_nop 0
	v_pk_mul_f32 v[46:47], v[42:43], v[0:1]
	v_pk_fma_f32 v[0:1], v[42:43], v[0:1], 1.0 op_sel_hi:[1,1,0] neg_lo:[1,0,0] neg_hi:[1,0,0]
	v_mul_f32_e64 v43, |v41|, s1
	v_cndmask_b32_e32 v1, v47, v1, vcc
	v_cmp_le_f32_e32 vcc, 0, v38
	s_nop 1
	v_cndmask_b32_e32 v0, v46, v0, vcc
	v_pk_mul_f32 v[0:1], v[38:39], v[0:1]
	v_mul_f32_e64 v39, |v40|, s1
	v_pk_mul_f32 v[0:1], v[204:205], v[0:1] op_sel_hi:[0,1]
	v_cvt_pk_f16_f32 v38, v0, v1
	v_fma_f32 v0, v39, s3, 1.0
	v_fma_f32 v1, v43, s3, 1.0
	v_rcp_f32_e32 v0, v0
	v_rcp_f32_e32 v1, v1
	v_mul_f32_e64 v39, v39, -v39
	v_mul_f32_e32 v39, 0x3fb8aa3b, v39
	v_exp_f32_e32 v42, v39
	v_pk_fma_f32 v[46:47], v[0:1], s[0:1], v[44:45] op_sel_hi:[1,0,0]
	v_mul_f32_e64 v39, v43, -v43
	v_mul_f32_e32 v39, 0x3fb8aa3b, v39
	v_pk_fma_f32 v[46:47], v[46:47], v[0:1], s[2:3] op_sel_hi:[1,1,0]
	v_exp_f32_e32 v43, v39
	v_pk_fma_f32 v[46:47], v[46:47], v[0:1], s[4:5] op_sel_hi:[1,1,0]
	v_cmp_le_f32_e32 vcc, 0, v41
	v_pk_fma_f32 v[46:47], v[46:47], v[0:1], s[6:7] op_sel_hi:[1,1,0]
	s_nop 0
	v_pk_mul_f32 v[0:1], v[0:1], v[46:47]
	s_nop 0
	v_pk_mul_f32 v[0:1], v[0:1], 0.5 op_sel_hi:[1,0]
	s_nop 0
	v_pk_mul_f32 v[46:47], v[42:43], v[0:1]
	v_pk_fma_f32 v[0:1], v[42:43], v[0:1], 1.0 op_sel_hi:[1,1,0] neg_lo:[1,0,0] neg_hi:[1,0,0]
	s_nop 0
	v_cndmask_b32_e32 v1, v47, v1, vcc
	v_cmp_le_f32_e32 vcc, 0, v40
	s_nop 1
	v_cndmask_b32_e32 v0, v46, v0, vcc
	v_pk_mul_f32 v[0:1], v[40:41], v[0:1]
	v_mul_f32_e64 v40, |v34|, s1
	v_pk_mul_f32 v[0:1], v[204:205], v[0:1] op_sel_hi:[0,1]
	v_mul_f32_e64 v41, |v35|, s1
	v_cvt_pk_f16_f32 v39, v0, v1
	v_fma_f32 v0, v40, s3, 1.0
	v_fma_f32 v1, v41, s3, 1.0
	v_rcp_f32_e32 v0, v0
	v_rcp_f32_e32 v1, v1
	v_mul_f32_e64 v40, v40, -v40
	v_mul_f32_e64 v41, v41, -v41
	v_mul_f32_e32 v40, 0x3fb8aa3b, v40
	v_pk_fma_f32 v[42:43], v[0:1], s[0:1], v[44:45] op_sel_hi:[1,0,0]
	v_mul_f32_e32 v41, 0x3fb8aa3b, v41
	v_pk_fma_f32 v[42:43], v[42:43], v[0:1], s[2:3] op_sel_hi:[1,1,0]
	v_exp_f32_e32 v40, v40
	v_exp_f32_e32 v41, v41
	v_pk_fma_f32 v[42:43], v[42:43], v[0:1], s[4:5] op_sel_hi:[1,1,0]
	v_cmp_le_f32_e32 vcc, 0, v35
	v_pk_fma_f32 v[42:43], v[42:43], v[0:1], s[6:7] op_sel_hi:[1,1,0]
	s_nop 0
	v_pk_mul_f32 v[0:1], v[0:1], v[42:43]
	s_nop 0
	v_pk_mul_f32 v[0:1], v[0:1], 0.5 op_sel_hi:[1,0]
	s_nop 0
	v_pk_mul_f32 v[42:43], v[40:41], v[0:1]
	v_pk_fma_f32 v[0:1], v[40:41], v[0:1], 1.0 op_sel_hi:[1,1,0] neg_lo:[1,0,0] neg_hi:[1,0,0]
	s_nop 0
	v_cndmask_b32_e32 v1, v43, v1, vcc
	v_cmp_le_f32_e32 vcc, 0, v34
	s_nop 1
	v_cndmask_b32_e32 v0, v42, v0, vcc
	v_pk_mul_f32 v[0:1], v[34:35], v[0:1]
	v_mul_f32_e64 v34, |v36|, s1
	v_pk_mul_f32 v[0:1], v[204:205], v[0:1] op_sel_hi:[0,1]
	v_mul_f32_e64 v35, |v37|, s1
	v_cvt_pk_f16_f32 v40, v0, v1
	v_fma_f32 v0, v34, s3, 1.0
	v_fma_f32 v1, v35, s3, 1.0
	v_rcp_f32_e32 v0, v0
	v_rcp_f32_e32 v1, v1
	v_mul_f32_e64 v34, v34, -v34
	v_mul_f32_e64 v35, v35, -v35
	v_mul_f32_e32 v34, 0x3fb8aa3b, v34
	v_pk_fma_f32 v[42:43], v[0:1], s[0:1], v[44:45] op_sel_hi:[1,0,0]
	v_mul_f32_e32 v35, 0x3fb8aa3b, v35
	v_pk_fma_f32 v[42:43], v[42:43], v[0:1], s[2:3] op_sel_hi:[1,1,0]
	v_exp_f32_e32 v34, v34
	v_exp_f32_e32 v35, v35
	v_pk_fma_f32 v[42:43], v[42:43], v[0:1], s[4:5] op_sel_hi:[1,1,0]
	v_cmp_le_f32_e32 vcc, 0, v37
	v_pk_fma_f32 v[42:43], v[42:43], v[0:1], s[6:7] op_sel_hi:[1,1,0]
	v_permlane16_swap_b32_e32 v38, v40
	v_pk_mul_f32 v[0:1], v[0:1], v[42:43]
	s_nop 0
	v_pk_mul_f32 v[0:1], v[0:1], 0.5 op_sel_hi:[1,0]
	s_nop 0
	v_pk_mul_f32 v[42:43], v[34:35], v[0:1]
	v_pk_fma_f32 v[0:1], v[34:35], v[0:1], 1.0 op_sel_hi:[1,1,0] neg_lo:[1,0,0] neg_hi:[1,0,0]
	s_nop 0
	v_cndmask_b32_e32 v1, v43, v1, vcc
	v_cmp_le_f32_e32 vcc, 0, v36
	s_nop 1
	v_cndmask_b32_e32 v0, v42, v0, vcc
	v_pk_mul_f32 v[0:1], v[36:37], v[0:1]
	v_cmp_lt_i32_e32 vcc, -1, v202
	v_pk_mul_f32 v[0:1], v[204:205], v[0:1] op_sel_hi:[0,1]
	v_cvt_pk_f16_f32 v41, v0, v1
	s_nop 1
	v_permlane16_swap_b32_e32 v39, v41
	s_and_saveexec_b64 s[10:11], vcc
	s_cbranch_execz .LBB2_124
	v_mov_b32_e32 v203, 0
	v_lshlrev_b64 v[0:1], 10, v[202:203]
	v_lshl_add_u64 v[0:1], v[78:79], 0, v[0:1]
	global_store_dwordx4 v[0:1], v[38:41], off sc1
.LBB2_124:
	s_or_b64 exec, exec, s[10:11]
	v_mul_f32_e64 v1, |v30|, s1
	v_mul_f32_e64 v35, |v31|, s1
	v_fma_f32 v0, v1, s3, 1.0
	v_mul_f32_e64 v34, v1, -v1
	v_fma_f32 v1, v35, s3, 1.0
	v_rcp_f32_e32 v0, v0
	v_rcp_f32_e32 v1, v1
	v_mov_b64_e32 v[36:37], s[8:9]
	v_mul_f32_e64 v35, v35, -v35
	v_mul_f32_e32 v34, 0x3fb8aa3b, v34
	v_pk_fma_f32 v[38:39], v[0:1], s[0:1], v[36:37] op_sel_hi:[1,0,0]
	v_mul_f32_e32 v35, 0x3fb8aa3b, v35
	v_pk_fma_f32 v[38:39], v[38:39], v[0:1], s[2:3] op_sel_hi:[1,1,0]
	v_exp_f32_e32 v34, v34
	v_exp_f32_e32 v35, v35
	v_pk_fma_f32 v[38:39], v[38:39], v[0:1], s[4:5] op_sel_hi:[1,1,0]
	v_cmp_le_f32_e32 vcc, 0, v31
	v_pk_fma_f32 v[38:39], v[38:39], v[0:1], s[6:7] op_sel_hi:[1,1,0]
	s_nop 0
	v_pk_mul_f32 v[0:1], v[0:1], v[38:39]
	s_nop 0
	v_pk_mul_f32 v[0:1], v[0:1], 0.5 op_sel_hi:[1,0]
	s_nop 0
	v_pk_mul_f32 v[38:39], v[34:35], v[0:1]
	v_pk_fma_f32 v[0:1], v[34:35], v[0:1], 1.0 op_sel_hi:[1,1,0] neg_lo:[1,0,0] neg_hi:[1,0,0]
	v_mul_f32_e64 v35, |v33|, s1
	v_cndmask_b32_e32 v1, v39, v1, vcc
	v_cmp_le_f32_e32 vcc, 0, v30
	s_nop 1
	v_cndmask_b32_e32 v0, v38, v0, vcc
	v_pk_mul_f32 v[0:1], v[30:31], v[0:1]
	v_mul_f32_e64 v31, |v32|, s1
	v_pk_mul_f32 v[0:1], v[200:201], v[0:1] op_sel_hi:[0,1]
	v_cvt_pk_f16_f32 v30, v0, v1
	v_fma_f32 v0, v31, s3, 1.0
	v_fma_f32 v1, v35, s3, 1.0
	v_rcp_f32_e32 v0, v0
	v_rcp_f32_e32 v1, v1
	v_mul_f32_e64 v31, v31, -v31
	v_mul_f32_e32 v31, 0x3fb8aa3b, v31
	v_exp_f32_e32 v34, v31
	v_pk_fma_f32 v[38:39], v[0:1], s[0:1], v[36:37] op_sel_hi:[1,0,0]
	v_mul_f32_e64 v31, v35, -v35
	v_mul_f32_e32 v31, 0x3fb8aa3b, v31
	v_pk_fma_f32 v[38:39], v[38:39], v[0:1], s[2:3] op_sel_hi:[1,1,0]
	v_exp_f32_e32 v35, v31
	v_pk_fma_f32 v[38:39], v[38:39], v[0:1], s[4:5] op_sel_hi:[1,1,0]
	v_cmp_le_f32_e32 vcc, 0, v33
	v_pk_fma_f32 v[38:39], v[38:39], v[0:1], s[6:7] op_sel_hi:[1,1,0]
	s_nop 0
	v_pk_mul_f32 v[0:1], v[0:1], v[38:39]
	s_nop 0
	v_pk_mul_f32 v[0:1], v[0:1], 0.5 op_sel_hi:[1,0]
	s_nop 0
	v_pk_mul_f32 v[38:39], v[34:35], v[0:1]
	v_pk_fma_f32 v[0:1], v[34:35], v[0:1], 1.0 op_sel_hi:[1,1,0] neg_lo:[1,0,0] neg_hi:[1,0,0]
	s_nop 0
	v_cndmask_b32_e32 v1, v39, v1, vcc
	v_cmp_le_f32_e32 vcc, 0, v32
	s_nop 1
	v_cndmask_b32_e32 v0, v38, v0, vcc
	v_pk_mul_f32 v[0:1], v[32:33], v[0:1]
	v_mul_f32_e64 v32, |v26|, s1
	v_pk_mul_f32 v[0:1], v[200:201], v[0:1] op_sel_hi:[0,1]
	v_mul_f32_e64 v33, |v27|, s1
	v_cvt_pk_f16_f32 v31, v0, v1
	v_fma_f32 v0, v32, s3, 1.0
	v_fma_f32 v1, v33, s3, 1.0
	v_rcp_f32_e32 v0, v0
	v_rcp_f32_e32 v1, v1
	v_mul_f32_e64 v32, v32, -v32
	v_mul_f32_e64 v33, v33, -v33
	v_mul_f32_e32 v32, 0x3fb8aa3b, v32
	v_pk_fma_f32 v[34:35], v[0:1], s[0:1], v[36:37] op_sel_hi:[1,0,0]
	v_mul_f32_e32 v33, 0x3fb8aa3b, v33
	v_pk_fma_f32 v[34:35], v[34:35], v[0:1], s[2:3] op_sel_hi:[1,1,0]
	v_exp_f32_e32 v32, v32
	v_exp_f32_e32 v33, v33
	v_pk_fma_f32 v[34:35], v[34:35], v[0:1], s[4:5] op_sel_hi:[1,1,0]
	v_cmp_le_f32_e32 vcc, 0, v27
	v_pk_fma_f32 v[34:35], v[34:35], v[0:1], s[6:7] op_sel_hi:[1,1,0]
	s_nop 0
	v_pk_mul_f32 v[0:1], v[0:1], v[34:35]
	s_nop 0
	v_pk_mul_f32 v[0:1], v[0:1], 0.5 op_sel_hi:[1,0]
	s_nop 0
	v_pk_mul_f32 v[34:35], v[32:33], v[0:1]
	v_pk_fma_f32 v[0:1], v[32:33], v[0:1], 1.0 op_sel_hi:[1,1,0] neg_lo:[1,0,0] neg_hi:[1,0,0]
	s_nop 0
	v_cndmask_b32_e32 v1, v35, v1, vcc
	v_cmp_le_f32_e32 vcc, 0, v26
	s_nop 1
	v_cndmask_b32_e32 v0, v34, v0, vcc
	v_pk_mul_f32 v[0:1], v[26:27], v[0:1]
	v_mul_f32_e64 v26, |v28|, s1
	v_pk_mul_f32 v[0:1], v[200:201], v[0:1] op_sel_hi:[0,1]
	v_mul_f32_e64 v27, |v29|, s1
	v_cvt_pk_f16_f32 v32, v0, v1
	v_fma_f32 v0, v26, s3, 1.0
	v_fma_f32 v1, v27, s3, 1.0
	v_rcp_f32_e32 v0, v0
	v_rcp_f32_e32 v1, v1
	v_mul_f32_e64 v26, v26, -v26
	v_mul_f32_e64 v27, v27, -v27
	v_mul_f32_e32 v26, 0x3fb8aa3b, v26
	v_pk_fma_f32 v[34:35], v[0:1], s[0:1], v[36:37] op_sel_hi:[1,0,0]
	v_mul_f32_e32 v27, 0x3fb8aa3b, v27
	v_pk_fma_f32 v[34:35], v[34:35], v[0:1], s[2:3] op_sel_hi:[1,1,0]
	v_exp_f32_e32 v26, v26
	v_exp_f32_e32 v27, v27
	v_pk_fma_f32 v[34:35], v[34:35], v[0:1], s[4:5] op_sel_hi:[1,1,0]
	v_cmp_le_f32_e32 vcc, 0, v29
	v_pk_fma_f32 v[34:35], v[34:35], v[0:1], s[6:7] op_sel_hi:[1,1,0]
	v_permlane16_swap_b32_e32 v30, v32
	v_pk_mul_f32 v[0:1], v[0:1], v[34:35]
	s_nop 0
	v_pk_mul_f32 v[0:1], v[0:1], 0.5 op_sel_hi:[1,0]
	s_nop 0
	v_pk_mul_f32 v[34:35], v[26:27], v[0:1]
	v_pk_fma_f32 v[0:1], v[26:27], v[0:1], 1.0 op_sel_hi:[1,1,0] neg_lo:[1,0,0] neg_hi:[1,0,0]
	s_nop 0
	v_cndmask_b32_e32 v1, v35, v1, vcc
	v_cmp_le_f32_e32 vcc, 0, v28
	s_nop 1
	v_cndmask_b32_e32 v0, v34, v0, vcc
	v_pk_mul_f32 v[0:1], v[28:29], v[0:1]
	v_cmp_lt_i32_e32 vcc, -1, v198
	v_pk_mul_f32 v[0:1], v[200:201], v[0:1] op_sel_hi:[0,1]
	v_cvt_pk_f16_f32 v33, v0, v1
	s_nop 1
	v_permlane16_swap_b32_e32 v31, v33
	s_and_saveexec_b64 s[0:1], vcc
	s_cbranch_execz .LBB2_126
	v_mov_b32_e32 v199, 0
	v_lshlrev_b64 v[0:1], 10, v[198:199]
	v_lshl_add_u64 v[0:1], v[78:79], 0, v[0:1]
	global_store_dwordx4 v[0:1], v[30:33], off sc1
.LBB2_126:
	s_or_b64 exec, exec, s[0:1]
	s_mov_b32 s1, 0x3f3504f3
	v_mul_f32_e64 v1, |v22|, s1
	v_fma_f32 v0, v1, s3, 1.0
	v_mul_f32_e64 v1, v1, -v1
	v_mul_f32_e32 v1, 0x3fb8aa3b, v1
	v_mul_f32_e64 v27, |v23|, s1
	v_exp_f32_e32 v26, v1
	v_fma_f32 v1, v27, s3, 1.0
	v_rcp_f32_e32 v0, v0
	v_rcp_f32_e32 v1, v1
	s_mov_b32 s0, 0x3f87dc22
	v_mov_b64_e32 v[28:29], s[8:9]
	v_mul_f32_e64 v27, v27, -v27
	v_pk_fma_f32 v[30:31], v[0:1], s[0:1], v[28:29] op_sel_hi:[1,0,0]
	v_mul_f32_e32 v27, 0x3fb8aa3b, v27
	v_pk_fma_f32 v[30:31], v[30:31], v[0:1], s[2:3] op_sel_hi:[1,1,0]
	v_exp_f32_e32 v27, v27
	v_pk_fma_f32 v[30:31], v[30:31], v[0:1], s[4:5] op_sel_hi:[1,1,0]
	v_cmp_le_f32_e32 vcc, 0, v23
	v_pk_fma_f32 v[30:31], v[30:31], v[0:1], s[6:7] op_sel_hi:[1,1,0]
	s_nop 0
	v_pk_mul_f32 v[0:1], v[0:1], v[30:31]
	s_nop 0
	v_pk_mul_f32 v[0:1], v[0:1], 0.5 op_sel_hi:[1,0]
	s_nop 0
	v_pk_mul_f32 v[30:31], v[26:27], v[0:1]
	v_pk_fma_f32 v[0:1], v[26:27], v[0:1], 1.0 op_sel_hi:[1,1,0] neg_lo:[1,0,0] neg_hi:[1,0,0]
	v_mul_f32_e64 v27, |v25|, s1
	v_cndmask_b32_e32 v1, v31, v1, vcc
	v_cmp_le_f32_e32 vcc, 0, v22
	s_nop 1
	v_cndmask_b32_e32 v0, v30, v0, vcc
	v_pk_mul_f32 v[0:1], v[22:23], v[0:1]
	v_mul_f32_e64 v23, |v24|, s1
	v_pk_mul_f32 v[0:1], v[196:197], v[0:1] op_sel_hi:[0,1]
	v_cvt_pk_f16_f32 v22, v0, v1
	v_fma_f32 v0, v23, s3, 1.0
	v_fma_f32 v1, v27, s3, 1.0
	v_rcp_f32_e32 v0, v0
	v_rcp_f32_e32 v1, v1
	v_mul_f32_e64 v23, v23, -v23
	v_mul_f32_e32 v23, 0x3fb8aa3b, v23
	v_exp_f32_e32 v26, v23
	v_pk_fma_f32 v[30:31], v[0:1], s[0:1], v[28:29] op_sel_hi:[1,0,0]
	v_mul_f32_e64 v23, v27, -v27
	v_mul_f32_e32 v23, 0x3fb8aa3b, v23
	v_pk_fma_f32 v[30:31], v[30:31], v[0:1], s[2:3] op_sel_hi:[1,1,0]
	v_exp_f32_e32 v27, v23
	v_pk_fma_f32 v[30:31], v[30:31], v[0:1], s[4:5] op_sel_hi:[1,1,0]
	v_cmp_le_f32_e32 vcc, 0, v25
	v_pk_fma_f32 v[30:31], v[30:31], v[0:1], s[6:7] op_sel_hi:[1,1,0]
	s_nop 0
	v_pk_mul_f32 v[0:1], v[0:1], v[30:31]
	s_nop 0
	v_pk_mul_f32 v[0:1], v[0:1], 0.5 op_sel_hi:[1,0]
	s_nop 0
	v_pk_mul_f32 v[30:31], v[26:27], v[0:1]
	v_pk_fma_f32 v[0:1], v[26:27], v[0:1], 1.0 op_sel_hi:[1,1,0] neg_lo:[1,0,0] neg_hi:[1,0,0]
	s_nop 0
	v_cndmask_b32_e32 v1, v31, v1, vcc
	v_cmp_le_f32_e32 vcc, 0, v24
	s_nop 1
	v_cndmask_b32_e32 v0, v30, v0, vcc
	v_pk_mul_f32 v[0:1], v[24:25], v[0:1]
	v_mul_f32_e64 v24, |v18|, s1
	v_pk_mul_f32 v[0:1], v[196:197], v[0:1] op_sel_hi:[0,1]
	v_mul_f32_e64 v25, |v19|, s1
	v_cvt_pk_f16_f32 v23, v0, v1
	v_fma_f32 v0, v24, s3, 1.0
	v_fma_f32 v1, v25, s3, 1.0
	v_rcp_f32_e32 v0, v0
	v_rcp_f32_e32 v1, v1
	v_mul_f32_e64 v24, v24, -v24
	v_mul_f32_e64 v25, v25, -v25
	v_mul_f32_e32 v24, 0x3fb8aa3b, v24
	v_pk_fma_f32 v[26:27], v[0:1], s[0:1], v[28:29] op_sel_hi:[1,0,0]
	v_mul_f32_e32 v25, 0x3fb8aa3b, v25
	v_pk_fma_f32 v[26:27], v[26:27], v[0:1], s[2:3] op_sel_hi:[1,1,0]
	v_exp_f32_e32 v24, v24
	v_exp_f32_e32 v25, v25
	v_pk_fma_f32 v[26:27], v[26:27], v[0:1], s[4:5] op_sel_hi:[1,1,0]
	v_cmp_le_f32_e32 vcc, 0, v19
	v_pk_fma_f32 v[26:27], v[26:27], v[0:1], s[6:7] op_sel_hi:[1,1,0]
	s_nop 0
	v_pk_mul_f32 v[0:1], v[0:1], v[26:27]
	s_nop 0
	v_pk_mul_f32 v[0:1], v[0:1], 0.5 op_sel_hi:[1,0]
	s_nop 0
	v_pk_mul_f32 v[26:27], v[24:25], v[0:1]
	v_pk_fma_f32 v[0:1], v[24:25], v[0:1], 1.0 op_sel_hi:[1,1,0] neg_lo:[1,0,0] neg_hi:[1,0,0]
	s_nop 0
	v_cndmask_b32_e32 v1, v27, v1, vcc
	v_cmp_le_f32_e32 vcc, 0, v18
	s_nop 1
	v_cndmask_b32_e32 v0, v26, v0, vcc
	v_pk_mul_f32 v[0:1], v[18:19], v[0:1]
	v_mul_f32_e64 v18, |v20|, s1
	v_pk_mul_f32 v[0:1], v[196:197], v[0:1] op_sel_hi:[0,1]
	v_mul_f32_e64 v19, |v21|, s1
	v_cvt_pk_f16_f32 v24, v0, v1
	v_fma_f32 v0, v18, s3, 1.0
	v_fma_f32 v1, v19, s3, 1.0
	v_rcp_f32_e32 v0, v0
	v_rcp_f32_e32 v1, v1
	v_mul_f32_e64 v18, v18, -v18
	v_mul_f32_e64 v19, v19, -v19
	v_mul_f32_e32 v18, 0x3fb8aa3b, v18
	v_pk_fma_f32 v[26:27], v[0:1], s[0:1], v[28:29] op_sel_hi:[1,0,0]
	v_mul_f32_e32 v19, 0x3fb8aa3b, v19
	v_pk_fma_f32 v[26:27], v[26:27], v[0:1], s[2:3] op_sel_hi:[1,1,0]
	v_exp_f32_e32 v18, v18
	v_exp_f32_e32 v19, v19
	v_pk_fma_f32 v[26:27], v[26:27], v[0:1], s[4:5] op_sel_hi:[1,1,0]
	v_cmp_le_f32_e32 vcc, 0, v21
	v_pk_fma_f32 v[26:27], v[26:27], v[0:1], s[6:7] op_sel_hi:[1,1,0]
	v_permlane16_swap_b32_e32 v22, v24
	v_pk_mul_f32 v[0:1], v[0:1], v[26:27]
	s_nop 0
	v_pk_mul_f32 v[0:1], v[0:1], 0.5 op_sel_hi:[1,0]
	s_nop 0
	v_pk_mul_f32 v[26:27], v[18:19], v[0:1]
	v_pk_fma_f32 v[0:1], v[18:19], v[0:1], 1.0 op_sel_hi:[1,1,0] neg_lo:[1,0,0] neg_hi:[1,0,0]
	s_nop 0
	v_cndmask_b32_e32 v1, v27, v1, vcc
	v_cmp_le_f32_e32 vcc, 0, v20
	s_nop 1
	v_cndmask_b32_e32 v0, v26, v0, vcc
	v_pk_mul_f32 v[0:1], v[20:21], v[0:1]
	v_cmp_lt_i32_e32 vcc, -1, v194
	v_pk_mul_f32 v[0:1], v[196:197], v[0:1] op_sel_hi:[0,1]
	v_cvt_pk_f16_f32 v25, v0, v1
	s_nop 1
	v_permlane16_swap_b32_e32 v23, v25
	s_and_saveexec_b64 s[10:11], vcc
	s_cbranch_execz .LBB2_128
	v_mov_b32_e32 v195, 0
	v_lshlrev_b64 v[0:1], 10, v[194:195]
	v_lshl_add_u64 v[0:1], v[78:79], 0, v[0:1]
	global_store_dwordx4 v[0:1], v[22:25], off sc1
.LBB2_128:
	s_or_b64 exec, exec, s[10:11]
	v_mul_f32_e64 v1, |v14|, s1
	v_mul_f32_e64 v19, |v15|, s1
	v_fma_f32 v0, v1, s3, 1.0
	v_mul_f32_e64 v18, v1, -v1
	v_fma_f32 v1, v19, s3, 1.0
	v_rcp_f32_e32 v0, v0
	v_rcp_f32_e32 v1, v1
	v_mov_b64_e32 v[20:21], s[8:9]
	v_mul_f32_e64 v19, v19, -v19
	v_mul_f32_e32 v18, 0x3fb8aa3b, v18
	v_pk_fma_f32 v[22:23], v[0:1], s[0:1], v[20:21] op_sel_hi:[1,0,0]
	v_mul_f32_e32 v19, 0x3fb8aa3b, v19
	v_pk_fma_f32 v[22:23], v[22:23], v[0:1], s[2:3] op_sel_hi:[1,1,0]
	v_exp_f32_e32 v18, v18
	v_exp_f32_e32 v19, v19
	v_pk_fma_f32 v[22:23], v[22:23], v[0:1], s[4:5] op_sel_hi:[1,1,0]
	v_cmp_le_f32_e32 vcc, 0, v15
	v_pk_fma_f32 v[22:23], v[22:23], v[0:1], s[6:7] op_sel_hi:[1,1,0]
	s_nop 0
	v_pk_mul_f32 v[0:1], v[0:1], v[22:23]
	s_nop 0
	v_pk_mul_f32 v[0:1], v[0:1], 0.5 op_sel_hi:[1,0]
	s_nop 0
	v_pk_mul_f32 v[22:23], v[18:19], v[0:1]
	v_pk_fma_f32 v[0:1], v[18:19], v[0:1], 1.0 op_sel_hi:[1,1,0] neg_lo:[1,0,0] neg_hi:[1,0,0]
	v_mul_f32_e64 v19, |v17|, s1
	v_cndmask_b32_e32 v1, v23, v1, vcc
	v_cmp_le_f32_e32 vcc, 0, v14
	s_nop 1
	v_cndmask_b32_e32 v0, v22, v0, vcc
	v_pk_mul_f32 v[0:1], v[14:15], v[0:1]
	v_mul_f32_e64 v15, |v16|, s1
	v_pk_mul_f32 v[0:1], v[192:193], v[0:1] op_sel_hi:[0,1]
	v_cvt_pk_f16_f32 v14, v0, v1
	v_fma_f32 v0, v15, s3, 1.0
	v_fma_f32 v1, v19, s3, 1.0
	v_rcp_f32_e32 v0, v0
	v_rcp_f32_e32 v1, v1
	v_mul_f32_e64 v15, v15, -v15
	v_mul_f32_e32 v15, 0x3fb8aa3b, v15
	v_exp_f32_e32 v18, v15
	v_pk_fma_f32 v[22:23], v[0:1], s[0:1], v[20:21] op_sel_hi:[1,0,0]
	v_mul_f32_e64 v15, v19, -v19
	v_mul_f32_e32 v15, 0x3fb8aa3b, v15
	v_pk_fma_f32 v[22:23], v[22:23], v[0:1], s[2:3] op_sel_hi:[1,1,0]
	v_exp_f32_e32 v19, v15
	v_pk_fma_f32 v[22:23], v[22:23], v[0:1], s[4:5] op_sel_hi:[1,1,0]
	v_cmp_le_f32_e32 vcc, 0, v17
	v_pk_fma_f32 v[22:23], v[22:23], v[0:1], s[6:7] op_sel_hi:[1,1,0]
	s_nop 0
	v_pk_mul_f32 v[0:1], v[0:1], v[22:23]
	s_nop 0
	v_pk_mul_f32 v[0:1], v[0:1], 0.5 op_sel_hi:[1,0]
	s_nop 0
	v_pk_mul_f32 v[22:23], v[18:19], v[0:1]
	v_pk_fma_f32 v[0:1], v[18:19], v[0:1], 1.0 op_sel_hi:[1,1,0] neg_lo:[1,0,0] neg_hi:[1,0,0]
	s_nop 0
	v_cndmask_b32_e32 v1, v23, v1, vcc
	v_cmp_le_f32_e32 vcc, 0, v16
	s_nop 1
	v_cndmask_b32_e32 v0, v22, v0, vcc
	v_pk_mul_f32 v[0:1], v[16:17], v[0:1]
	v_mul_f32_e64 v16, |v10|, s1
	v_pk_mul_f32 v[0:1], v[192:193], v[0:1] op_sel_hi:[0,1]
	v_mul_f32_e64 v17, |v11|, s1
	v_cvt_pk_f16_f32 v15, v0, v1
	v_fma_f32 v0, v16, s3, 1.0
	v_fma_f32 v1, v17, s3, 1.0
	v_rcp_f32_e32 v0, v0
	v_rcp_f32_e32 v1, v1
	v_mul_f32_e64 v16, v16, -v16
	v_mul_f32_e64 v17, v17, -v17
	v_mul_f32_e32 v16, 0x3fb8aa3b, v16
	v_pk_fma_f32 v[18:19], v[0:1], s[0:1], v[20:21] op_sel_hi:[1,0,0]
	v_mul_f32_e32 v17, 0x3fb8aa3b, v17
	v_pk_fma_f32 v[18:19], v[18:19], v[0:1], s[2:3] op_sel_hi:[1,1,0]
	v_exp_f32_e32 v16, v16
	v_exp_f32_e32 v17, v17
	v_pk_fma_f32 v[18:19], v[18:19], v[0:1], s[4:5] op_sel_hi:[1,1,0]
	v_cmp_le_f32_e32 vcc, 0, v11
	v_pk_fma_f32 v[18:19], v[18:19], v[0:1], s[6:7] op_sel_hi:[1,1,0]
	s_nop 0
	v_pk_mul_f32 v[0:1], v[0:1], v[18:19]
	s_nop 0
	v_pk_mul_f32 v[0:1], v[0:1], 0.5 op_sel_hi:[1,0]
	s_nop 0
	v_pk_mul_f32 v[18:19], v[16:17], v[0:1]
	v_pk_fma_f32 v[0:1], v[16:17], v[0:1], 1.0 op_sel_hi:[1,1,0] neg_lo:[1,0,0] neg_hi:[1,0,0]
	s_nop 0
	v_cndmask_b32_e32 v1, v19, v1, vcc
	v_cmp_le_f32_e32 vcc, 0, v10
	s_nop 1
	v_cndmask_b32_e32 v0, v18, v0, vcc
	v_pk_mul_f32 v[0:1], v[10:11], v[0:1]
	v_mul_f32_e64 v10, |v12|, s1
	v_pk_mul_f32 v[0:1], v[192:193], v[0:1] op_sel_hi:[0,1]
	v_mul_f32_e64 v11, |v13|, s1
	v_cvt_pk_f16_f32 v16, v0, v1
	v_fma_f32 v0, v10, s3, 1.0
	v_fma_f32 v1, v11, s3, 1.0
	v_rcp_f32_e32 v0, v0
	v_rcp_f32_e32 v1, v1
	v_mul_f32_e64 v10, v10, -v10
	v_mul_f32_e64 v11, v11, -v11
	v_mul_f32_e32 v10, 0x3fb8aa3b, v10
	v_pk_fma_f32 v[18:19], v[0:1], s[0:1], v[20:21] op_sel_hi:[1,0,0]
	v_mul_f32_e32 v11, 0x3fb8aa3b, v11
	v_pk_fma_f32 v[18:19], v[18:19], v[0:1], s[2:3] op_sel_hi:[1,1,0]
	v_exp_f32_e32 v10, v10
	v_exp_f32_e32 v11, v11
	v_pk_fma_f32 v[18:19], v[18:19], v[0:1], s[4:5] op_sel_hi:[1,1,0]
	v_cmp_le_f32_e32 vcc, 0, v13
	v_pk_fma_f32 v[18:19], v[18:19], v[0:1], s[6:7] op_sel_hi:[1,1,0]
	v_permlane16_swap_b32_e32 v14, v16
	v_pk_mul_f32 v[0:1], v[0:1], v[18:19]
	s_nop 0
	v_pk_mul_f32 v[0:1], v[0:1], 0.5 op_sel_hi:[1,0]
	s_nop 0
	v_pk_mul_f32 v[18:19], v[10:11], v[0:1]
	v_pk_fma_f32 v[0:1], v[10:11], v[0:1], 1.0 op_sel_hi:[1,1,0] neg_lo:[1,0,0] neg_hi:[1,0,0]
	s_nop 0
	v_cndmask_b32_e32 v1, v19, v1, vcc
	v_cmp_le_f32_e32 vcc, 0, v12
	s_nop 1
	v_cndmask_b32_e32 v0, v18, v0, vcc
	v_pk_mul_f32 v[0:1], v[12:13], v[0:1]
	v_cmp_lt_i32_e32 vcc, -1, v190
	v_pk_mul_f32 v[0:1], v[192:193], v[0:1] op_sel_hi:[0,1]
	v_cvt_pk_f16_f32 v17, v0, v1
	s_nop 1
	v_permlane16_swap_b32_e32 v15, v17
	s_and_saveexec_b64 s[0:1], vcc
	s_cbranch_execz .LBB2_130
	v_mov_b32_e32 v191, 0
	v_lshlrev_b64 v[0:1], 10, v[190:191]
	v_lshl_add_u64 v[0:1], v[78:79], 0, v[0:1]
	global_store_dwordx4 v[0:1], v[14:17], off sc1
.LBB2_130:
	s_or_b64 exec, exec, s[0:1]
	s_mov_b32 s1, 0x3f3504f3
	v_mul_f32_e64 v1, |v6|, s1
	v_fma_f32 v0, v1, s3, 1.0
	v_mul_f32_e64 v1, v1, -v1
	v_mul_f32_e32 v1, 0x3fb8aa3b, v1
	v_mul_f32_e64 v11, |v7|, s1
	v_exp_f32_e32 v10, v1
	v_fma_f32 v1, v11, s3, 1.0
	v_rcp_f32_e32 v0, v0
	v_rcp_f32_e32 v1, v1
	s_mov_b32 s2, 0xbfba00e3
	s_mov_b32 s0, 0x3f87dc22
	v_mov_b64_e32 v[12:13], s[2:3]
	v_pk_fma_f32 v[14:15], v[0:1], s[0:1], v[12:13] op_sel_hi:[1,0,0]
	v_mul_f32_e64 v11, v11, -v11
	s_mov_b32 s2, 0x3fb5f0e3
	v_mul_f32_e32 v11, 0x3fb8aa3b, v11
	v_pk_fma_f32 v[14:15], v[14:15], v[0:1], s[2:3] op_sel_hi:[1,1,0]
	v_exp_f32_e32 v11, v11
	v_pk_fma_f32 v[14:15], v[14:15], v[0:1], s[4:5] op_sel_hi:[1,1,0]
	v_cmp_le_f32_e32 vcc, 0, v7
	v_pk_fma_f32 v[14:15], v[14:15], v[0:1], s[6:7] op_sel_hi:[1,1,0]
	s_nop 0
	v_pk_mul_f32 v[0:1], v[0:1], v[14:15]
	s_nop 0
	v_pk_mul_f32 v[0:1], v[0:1], 0.5 op_sel_hi:[1,0]
	s_nop 0
	v_pk_mul_f32 v[14:15], v[10:11], v[0:1]
	v_pk_fma_f32 v[0:1], v[10:11], v[0:1], 1.0 op_sel_hi:[1,1,0] neg_lo:[1,0,0] neg_hi:[1,0,0]
	v_mul_f32_e64 v11, |v9|, s1
	v_cndmask_b32_e32 v1, v15, v1, vcc
	v_cmp_le_f32_e32 vcc, 0, v6
	s_nop 1
	v_cndmask_b32_e32 v0, v14, v0, vcc
	v_pk_mul_f32 v[0:1], v[6:7], v[0:1]
	v_fma_f32 v7, v11, s3, 1.0
	v_pk_mul_f32 v[0:1], v[188:189], v[0:1] op_sel_hi:[0,1]
	v_cvt_pk_f16_f32 v0, v0, v1
	v_mul_f32_e64 v1, |v8|, s1
	v_fma_f32 v6, v1, s3, 1.0
	v_rcp_f32_e32 v6, v6
	v_rcp_f32_e32 v7, v7
	v_mul_f32_e64 v1, v1, -v1
	v_mul_f32_e32 v1, 0x3fb8aa3b, v1
	v_exp_f32_e32 v10, v1
	v_pk_fma_f32 v[14:15], v[6:7], s[0:1], v[12:13] op_sel_hi:[1,0,0]
	v_mul_f32_e64 v1, v11, -v11
	v_mul_f32_e32 v1, 0x3fb8aa3b, v1
	v_pk_fma_f32 v[14:15], v[14:15], v[6:7], s[2:3] op_sel_hi:[1,1,0]
	v_exp_f32_e32 v11, v1
	v_pk_fma_f32 v[14:15], v[14:15], v[6:7], s[4:5] op_sel_hi:[1,1,0]
	v_cmp_le_f32_e32 vcc, 0, v9
	v_pk_fma_f32 v[14:15], v[14:15], v[6:7], s[6:7] op_sel_hi:[1,1,0]
	s_nop 0
	v_pk_mul_f32 v[6:7], v[6:7], v[14:15]
	s_nop 0
	v_pk_mul_f32 v[6:7], v[6:7], 0.5 op_sel_hi:[1,0]
	s_nop 0
	v_pk_mul_f32 v[14:15], v[10:11], v[6:7]
	v_pk_fma_f32 v[6:7], v[10:11], v[6:7], 1.0 op_sel_hi:[1,1,0] neg_lo:[1,0,0] neg_hi:[1,0,0]
	s_nop 0
	v_cndmask_b32_e32 v7, v15, v7, vcc
	v_cmp_le_f32_e32 vcc, 0, v8
	s_nop 1
	v_cndmask_b32_e32 v6, v14, v6, vcc
	v_pk_mul_f32 v[6:7], v[8:9], v[6:7]
	v_mul_f32_e64 v8, |v2|, s1
	v_pk_mul_f32 v[6:7], v[188:189], v[6:7] op_sel_hi:[0,1]
	v_mul_f32_e64 v9, |v3|, s1
	v_cvt_pk_f16_f32 v1, v6, v7
	v_fma_f32 v6, v8, s3, 1.0
	v_fma_f32 v7, v9, s3, 1.0
	v_rcp_f32_e32 v6, v6
	v_rcp_f32_e32 v7, v7
	v_mul_f32_e64 v8, v8, -v8
	v_mul_f32_e64 v9, v9, -v9
	v_mul_f32_e32 v8, 0x3fb8aa3b, v8
	v_pk_fma_f32 v[10:11], v[6:7], s[0:1], v[12:13] op_sel_hi:[1,0,0]
	v_mul_f32_e32 v9, 0x3fb8aa3b, v9
	v_pk_fma_f32 v[10:11], v[10:11], v[6:7], s[2:3] op_sel_hi:[1,1,0]
	v_exp_f32_e32 v8, v8
	v_exp_f32_e32 v9, v9
	v_pk_fma_f32 v[10:11], v[10:11], v[6:7], s[4:5] op_sel_hi:[1,1,0]
	v_cmp_le_f32_e32 vcc, 0, v3
	v_pk_fma_f32 v[10:11], v[10:11], v[6:7], s[6:7] op_sel_hi:[1,1,0]
	s_nop 0
	v_pk_mul_f32 v[6:7], v[6:7], v[10:11]
	s_nop 0
	v_pk_mul_f32 v[6:7], v[6:7], 0.5 op_sel_hi:[1,0]
	s_nop 0
	v_pk_mul_f32 v[10:11], v[8:9], v[6:7]
	v_pk_fma_f32 v[6:7], v[8:9], v[6:7], 1.0 op_sel_hi:[1,1,0] neg_lo:[1,0,0] neg_hi:[1,0,0]
	v_mul_f32_e64 v9, |v5|, s1
	v_cndmask_b32_e32 v7, v11, v7, vcc
	v_cmp_le_f32_e32 vcc, 0, v2
	s_nop 1
	v_cndmask_b32_e32 v6, v10, v6, vcc
	v_pk_mul_f32 v[2:3], v[2:3], v[6:7]
	v_fma_f32 v7, v9, s3, 1.0
	v_pk_mul_f32 v[2:3], v[188:189], v[2:3] op_sel_hi:[0,1]
	v_cvt_pk_f16_f32 v2, v2, v3
	v_mul_f32_e64 v3, |v4|, s1
	v_fma_f32 v6, v3, s3, 1.0
	v_rcp_f32_e32 v6, v6
	v_rcp_f32_e32 v7, v7
	v_mul_f32_e64 v3, v3, -v3
	v_mul_f32_e32 v3, 0x3fb8aa3b, v3
	v_exp_f32_e32 v8, v3
	v_pk_fma_f32 v[10:11], v[6:7], s[0:1], v[12:13] op_sel_hi:[1,0,0]
	v_mul_f32_e64 v3, v9, -v9
	v_mul_f32_e32 v3, 0x3fb8aa3b, v3
	v_pk_fma_f32 v[10:11], v[10:11], v[6:7], s[2:3] op_sel_hi:[1,1,0]
	v_exp_f32_e32 v9, v3
	v_pk_fma_f32 v[10:11], v[10:11], v[6:7], s[4:5] op_sel_hi:[1,1,0]
	v_cmp_le_f32_e32 vcc, 0, v5
	v_pk_fma_f32 v[10:11], v[10:11], v[6:7], s[6:7] op_sel_hi:[1,1,0]
	v_permlane16_swap_b32_e32 v0, v2
	v_pk_mul_f32 v[6:7], v[6:7], v[10:11]
	s_nop 0
	v_pk_mul_f32 v[6:7], v[6:7], 0.5 op_sel_hi:[1,0]
	s_nop 0
	v_pk_mul_f32 v[10:11], v[8:9], v[6:7]
	v_pk_fma_f32 v[6:7], v[8:9], v[6:7], 1.0 op_sel_hi:[1,1,0] neg_lo:[1,0,0] neg_hi:[1,0,0]
	s_nop 0
	v_cndmask_b32_e32 v7, v11, v7, vcc
	v_cmp_le_f32_e32 vcc, 0, v4
	s_nop 1
	v_cndmask_b32_e32 v6, v10, v6, vcc
	v_pk_mul_f32 v[4:5], v[4:5], v[6:7]
	v_cmp_lt_i32_e32 vcc, -1, v186
	v_pk_mul_f32 v[4:5], v[188:189], v[4:5] op_sel_hi:[0,1]
	v_cvt_pk_f16_f32 v3, v4, v5
	s_nop 1
	v_permlane16_swap_b32_e32 v1, v3
	s_and_saveexec_b64 s[0:1], vcc
	s_cbranch_execz .LBB2_132
	v_mov_b32_e32 v187, 0
	v_lshlrev_b64 v[4:5], 10, v[186:187]
	v_lshl_add_u64 v[4:5], v[78:79], 0, v[4:5]
	global_store_dwordx4 v[4:5], v[0:3], off sc1

	.amdhsa_kernel _Z8moe_gemmILi0EEvPKDF16_S1_PvPKyPKiPKfS1_
		.amdhsa_group_segment_fixed_size 0
		.amdhsa_private_segment_fixed_size 0
		.amdhsa_kernarg_size 56
		.amdhsa_user_sgpr_count 2
		.amdhsa_user_sgpr_dispatch_ptr 0
		.amdhsa_user_sgpr_queue_ptr 0
		.amdhsa_user_sgpr_kernarg_segment_ptr 1
		.amdhsa_user_sgpr_dispatch_id 0
		.amdhsa_user_sgpr_kernarg_preload_length 0
		.amdhsa_user_sgpr_kernarg_preload_offset 0
		.amdhsa_user_sgpr_private_segment_size 0
		.amdhsa_uses_dynamic_stack 0
		.amdhsa_enable_private_segment 0
		.amdhsa_system_sgpr_workgroup_id_x 1
		.amdhsa_system_sgpr_workgroup_id_y 0
		.amdhsa_system_sgpr_workgroup_id_z 0
		.amdhsa_system_sgpr_workgroup_info 0
		.amdhsa_system_vgpr_workitem_id 0
		.amdhsa_next_free_vgpr 248
		.amdhsa_next_free_sgpr 76
		.amdhsa_accum_offset 248
		.amdhsa_reserve_vcc 1
		.amdhsa_float_round_mode_32 0
		.amdhsa_float_round_mode_16_64 0
		.amdhsa_float_denorm_mode_32 3
		.amdhsa_float_denorm_mode_16_64 3
		.amdhsa_dx10_clamp 1
		.amdhsa_ieee_mode 1
		.amdhsa_fp16_overflow 0
		.amdhsa_tg_split 0
		.amdhsa_exception_fp_ieee_invalid_op 0
		.amdhsa_exception_fp_denorm_src 0
		.amdhsa_exception_fp_ieee_div_zero 0
		.amdhsa_exception_fp_ieee_overflow 0
		.amdhsa_exception_fp_ieee_underflow 0
		.amdhsa_exception_fp_ieee_inexact 0
		.amdhsa_exception_int_div_zero 0
	.end_amdhsa_kernel

.LBB3_35:
	s_abs_i32 s3, s26
	v_cvt_f32_u32_e32 v1, s3
	s_sub_i32 s11, 0, s3
	s_lshl_b32 s10, s19, 2
	s_add_i32 s15, s12, -1
	v_rcp_iflag_f32_e32 v1, v1
	s_sub_i32 s14, s18, s10
	s_add_i32 s10, s15, s26
	s_xor_b32 s16, s10, s26
	v_mul_f32_e32 v1, 0x4f7ffffe, v1
	v_cvt_u32_f32_e32 v1, v1
	s_abs_i32 s10, s10
	s_ashr_i32 s16, s16, 31
	v_lshlrev_b32_e32 v108, 4, v0
	v_readfirstlane_b32 s17, v1
	s_mul_i32 s11, s11, s17
	s_mul_hi_u32 s11, s17, s11
	s_add_i32 s17, s17, s11
	s_mul_hi_u32 s11, s10, s17
	s_mul_i32 s17, s11, s3
	s_sub_i32 s10, s10, s17
	s_add_i32 s18, s11, 1
	s_sub_i32 s17, s10, s3
	s_cmp_ge_u32 s10, s3
	s_cselect_b32 s11, s18, s11
	s_cselect_b32 s10, s17, s10
	s_add_i32 s17, s11, 1
	s_cmp_ge_u32 s10, s3
	s_cselect_b32 s3, s17, s11
	s_xor_b32 s3, s3, s16
	s_sub_i32 s16, s3, s16
	s_add_i32 s16, s16, 15
	s_and_b32 s17, s16, -16
	v_lshrrev_b32_e32 v1, 3, v0
	s_mul_i32 s19, s17, s2
	v_add_u32_e32 v7, s19, v1
	s_lshl_b32 s2, s13, 13
	s_or_b32 s18, s2, 0x1fff
	v_min_i32_e32 v2, s15, v7
	v_add_u32_e32 v4, 64, v7
	v_sub_u32_e32 v2, s18, v2
	v_min_i32_e32 v4, s15, v4
	v_ashrrev_i32_e32 v3, 31, v2
	v_sub_u32_e32 v4, s18, v4
	s_waitcnt lgkmcnt(0)
	v_lshl_add_u64 v[2:3], v[2:3], 2, s[8:9]
	v_ashrrev_i32_e32 v5, 31, v4
	v_lshl_add_u64 v[4:5], v[4:5], 2, s[8:9]
	global_load_dword v6, v[2:3], off
	global_load_dword v8, v[4:5], off
	v_add_u32_e32 v146, 0x80, v7
	v_min_i32_e32 v146, s15, v146
	v_sub_u32_e32 v146, s18, v146
	v_ashrrev_i32_e32 v147, 31, v146
	v_lshl_add_u64 v[146:147], v[146:147], 2, s[8:9]
	global_load_dword v146, v[146:147], off
	v_add_u32_e32 v109, 0, v108
	s_lshl_b32 s14, s14, 8
	v_add_u32_e32 v4, 0x5000, v109
	v_add_u32_e32 v5, 0x7000, v109
	s_ashr_i32 s30, s14, 31
	s_mov_b32 s11, 0
	v_readfirstlane_b32 s26, v4
	v_readfirstlane_b32 s27, v5
	s_lshl_b32 s10, s13, 10
	v_or_b32_e32 v4, s14, v1
	v_mov_b32_e32 v5, s30
	v_xor_b32_e32 v2, v1, v0
	s_add_i32 s13, 0, 0x12000
	v_lshl_add_u64 v[4:5], v[4:5], 0, s[10:11]
	v_lshlrev_b32_e32 v2, 4, v2
	v_add_u32_e32 v10, 0xb000, v109
	v_add_u32_e32 v110, s13, v108
	v_lshlrev_b64 v[4:5], 10, v[4:5]
	v_mov_b32_e32 v3, 0
	v_and_b32_e32 v2, 0x70, v2
	v_readfirstlane_b32 s29, v10
	v_add_u32_e32 v1, 0x2000, v110
	v_lshl_add_u64 v[10:11], s[6:7], 0, v[4:5]
	s_mov_b64 s[20:21], 0x10000
	v_add_u32_e32 v9, 0x9000, v109
	v_readfirstlane_b32 s10, v1
	v_or_b32_e32 v4, 0x20000, v4
	v_lshl_add_u64 v[100:101], v[10:11], 0, v[2:3]
	v_add_u32_e32 v1, 0x80, v7
	s_mov_b32 m0, s26
	v_readfirstlane_b32 s28, v9
	v_lshl_add_u64 v[4:5], s[6:7], 0, v[4:5]
	v_lshl_add_u64 v[98:99], v[100:101], 0, s[20:21]
	global_load_lds_dwordx4 v[100:101], off
	v_min_i32_e32 v1, s15, v1
	s_mov_b32 m0, s27
	s_mov_b64 s[22:23], 0x30000
	v_lshl_add_u64 v[96:97], v[4:5], 0, v[2:3]
	global_load_lds_dwordx4 v[98:99], off
	v_sub_u32_e32 v14, s18, v1
	s_mov_b32 m0, s28
	s_mov_b64 s[2:3], 0x80
	v_readfirstlane_b32 s13, v110
	v_lshl_add_u64 v[94:95], v[100:101], 0, s[22:23]
	global_load_lds_dwordx4 v[96:97], off
	v_ashrrev_i32_e32 v15, 31, v14
	s_mov_b32 m0, s29
	s_mov_b64 s[24:25], 0x10080
	v_lshl_add_u64 v[4:5], v[100:101], 0, s[2:3]
	global_load_lds_dwordx4 v[94:95], off
	v_lshl_add_u64 v[14:15], v[14:15], 2, s[8:9]
	s_mov_b32 m0, s13
	v_add_u32_e32 v1, 0x4000, v110
	v_lshl_add_u64 v[10:11], v[100:101], 0, s[24:25]
	global_load_lds_dwordx4 v[4:5], off
	s_mov_b32 m0, s10
	v_readfirstlane_b32 s6, v1
	global_load_lds_dwordx4 v[10:11], off
	s_mov_b32 m0, s6
	s_mov_b64 s[6:7], 0x30080
	v_add_u32_e32 v1, 0x6000, v110
	v_lshl_add_u64 v[12:13], v[96:97], 0, s[2:3]
	v_lshl_add_u64 v[10:11], v[100:101], 0, s[6:7]
	v_readfirstlane_b32 s6, v1
	global_load_lds_dwordx4 v[12:13], off
	s_mov_b32 m0, s6
	v_readfirstlane_b32 s6, v109
	v_add_u32_e32 v1, 0x2000, v109
	global_load_lds_dwordx4 v[10:11], off
	s_waitcnt vmcnt(8)
	v_mov_b32_e32 v4, v146
	v_ashrrev_i32_e32 v7, 31, v6
	v_lshlrev_b64 v[6:7], 10, v[6:7]
	v_ashrrev_i32_e32 v9, 31, v8
	v_lshl_add_u64 v[6:7], s[4:5], 0, v[6:7]
	v_lshl_add_u64 v[104:105], v[6:7], 0, v[2:3]
	v_lshlrev_b64 v[6:7], 10, v[8:9]
	v_lshl_add_u64 v[6:7], s[4:5], 0, v[6:7]
	s_mov_b32 m0, s6
	v_readfirstlane_b32 s6, v1
	v_lshl_add_u64 v[102:103], v[6:7], 0, v[2:3]
	global_load_lds_dwordx4 v[104:105], off
	s_mov_b32 m0, s6
	s_lshr_b32 s7, s16, 3
	global_load_lds_dwordx4 v[102:103], off
	v_readfirstlane_b32 s6, v0
	s_and_b32 s7, s7, 0x1ffffffe
	s_lshr_b32 s15, s6, 6
	s_add_i32 s7, s7, -16
	s_cmp_lt_i32 s15, s7
	v_ashrrev_i32_e32 v5, 31, v4
	v_lshlrev_b64 v[4:5], 10, v[4:5]
	v_lshl_add_u64 v[4:5], s[4:5], 0, v[4:5]
	s_cselect_b64 s[4:5], -1, 0
	s_cmp_ge_i32 s15, s7
	s_cselect_b64 s[10:11], -1, 0
	v_lshl_add_u64 v[106:107], v[4:5], 0, v[2:3]
	s_and_b64 vcc, exec, s[10:11]
	s_cbranch_vccnz .LBB3_37
	v_add_u32_e32 v1, 0x4000, v109
	s_nop 0
	v_readfirstlane_b32 s7, v1
	s_mov_b32 m0, s7
	s_nop 0
	global_load_lds_dwordx4 v[106:107], off

	.amdhsa_kernel _Z8moe_gemmILi1EEvPKDF16_S1_PvPKyPKiPKfS1_
		.amdhsa_group_segment_fixed_size 0
		.amdhsa_private_segment_fixed_size 0
		.amdhsa_kernarg_size 56
		.amdhsa_user_sgpr_count 2
		.amdhsa_user_sgpr_dispatch_ptr 0
		.amdhsa_user_sgpr_queue_ptr 0
		.amdhsa_user_sgpr_kernarg_segment_ptr 1
		.amdhsa_user_sgpr_dispatch_id 0
		.amdhsa_user_sgpr_kernarg_preload_length 0
		.amdhsa_user_sgpr_kernarg_preload_offset 0
		.amdhsa_user_sgpr_private_segment_size 0
		.amdhsa_uses_dynamic_stack 0
		.amdhsa_enable_private_segment 0
		.amdhsa_system_sgpr_workgroup_id_x 1
		.amdhsa_system_sgpr_workgroup_id_y 0
		.amdhsa_system_sgpr_workgroup_id_z 0
		.amdhsa_system_sgpr_workgroup_info 0
		.amdhsa_system_vgpr_workitem_id 0
		.amdhsa_next_free_vgpr 148
		.amdhsa_next_free_sgpr 62
		.amdhsa_accum_offset 148
		.amdhsa_reserve_vcc 1
		.amdhsa_float_round_mode_32 0
		.amdhsa_float_round_mode_16_64 0
		.amdhsa_float_denorm_mode_32 3
		.amdhsa_float_denorm_mode_16_64 3
		.amdhsa_dx10_clamp 1
		.amdhsa_ieee_mode 1
		.amdhsa_fp16_overflow 0
		.amdhsa_tg_split 0
		.amdhsa_exception_fp_ieee_invalid_op 0
		.amdhsa_exception_fp_denorm_src 0
		.amdhsa_exception_fp_ieee_div_zero 0
		.amdhsa_exception_fp_ieee_overflow 0
		.amdhsa_exception_fp_ieee_underflow 0
		.amdhsa_exception_fp_ieee_inexact 0
		.amdhsa_exception_int_div_zero 0
	.end_amdhsa_kernel

.LBB4_35:
	s_abs_i32 s3, s26
	v_cvt_f32_u32_e32 v1, s3
	s_sub_i32 s11, 0, s3
	s_lshl_b32 s10, s19, 2
	s_add_i32 s17, s12, -1
	v_rcp_iflag_f32_e32 v1, v1
	s_sub_i32 s24, s18, s10
	s_add_i32 s10, s17, s26
	s_xor_b32 s14, s10, s26
	v_mul_f32_e32 v1, 0x4f7ffffe, v1
	v_cvt_u32_f32_e32 v1, v1
	s_abs_i32 s10, s10
	s_ashr_i32 s14, s14, 31
	v_lshrrev_b32_e32 v7, 3, v0
	v_readfirstlane_b32 s15, v1
	s_mul_i32 s11, s11, s15
	s_mul_hi_u32 s11, s15, s11
	s_add_i32 s15, s15, s11
	s_mul_hi_u32 s11, s10, s15
	s_mul_i32 s15, s11, s3
	s_sub_i32 s10, s10, s15
	s_add_i32 s16, s11, 1
	s_sub_i32 s15, s10, s3
	s_cmp_ge_u32 s10, s3
	s_cselect_b32 s11, s16, s11
	s_cselect_b32 s10, s15, s10
	s_add_i32 s15, s11, 1
	s_cmp_ge_u32 s10, s3
	s_cselect_b32 s3, s15, s11
	s_xor_b32 s3, s3, s14
	s_sub_i32 s34, s3, s14
	s_add_i32 s34, s34, 15
	s_and_b32 s10, s34, -16
	s_mul_i32 s11, s10, s2
	v_add_u32_e32 v9, s11, v7
	s_lshl_b32 s16, s13, 13
	v_min_i32_e32 v1, s17, v9
	v_add_u32_e32 v2, s16, v1
	v_add_u32_e32 v1, 64, v9
	v_min_i32_e32 v1, s17, v1
	v_ashrrev_i32_e32 v3, 31, v2
	v_add_u32_e32 v4, s16, v1
	s_waitcnt lgkmcnt(0)
	v_lshl_add_u64 v[2:3], v[2:3], 2, s[8:9]
	v_ashrrev_i32_e32 v5, 31, v4
	v_lshl_add_u64 v[4:5], v[4:5], 2, s[8:9]
	global_load_dword v6, v[2:3], off
	global_load_dword v8, v[4:5], off
	v_add_u32_e32 v152, 0x80, v9
	v_min_i32_e32 v152, s17, v152
	v_add_u32_e32 v152, s16, v152
	v_ashrrev_i32_e32 v153, 31, v152
	v_lshl_add_u64 v[152:153], v[152:153], 2, s[8:9]
	global_load_dword v152, v[152:153], off
	v_lshlrev_b32_e32 v1, 4, v0
	v_add_u32_e32 v135, 0, v1
	s_lshl_b32 s14, s13, 10
	s_lshl_b32 s13, s24, 8
	v_add_u32_e32 v4, 0x5000, v135
	v_add_u32_e32 v5, 0x7000, v135
	s_ashr_i32 s29, s13, 31
	s_mov_b32 s15, 0
	v_readfirstlane_b32 s25, v4
	v_readfirstlane_b32 s26, v5
	v_or_b32_e32 v4, s13, v7
	v_mov_b32_e32 v5, s29
	v_xor_b32_e32 v2, v7, v0
	s_add_i32 s24, 0, 0x12000
	v_lshl_add_u64 v[4:5], v[4:5], 0, s[14:15]
	v_lshlrev_b32_e32 v2, 4, v2
	v_add_u32_e32 v10, 0x9000, v135
	v_add_u32_e32 v11, 0xb000, v135
	v_add_u32_e32 v136, s24, v1
	v_lshlrev_b64 v[4:5], 10, v[4:5]
	v_mov_b32_e32 v3, 0
	v_and_b32_e32 v2, 0x70, v2
	v_readfirstlane_b32 s27, v10
	v_readfirstlane_b32 s28, v11
	v_add_u32_e32 v7, 0x2000, v136
	v_lshl_add_u64 v[10:11], s[6:7], 0, v[4:5]
	s_mov_b64 s[18:19], 0x10000
	v_readfirstlane_b32 s14, v7
	v_or_b32_e32 v4, 0x20000, v4
	v_lshl_add_u64 v[116:117], v[10:11], 0, v[2:3]
	v_add_u32_e32 v7, 0x80, v9
	s_mov_b32 m0, s25
	v_lshl_add_u64 v[4:5], s[6:7], 0, v[4:5]
	v_lshl_add_u64 v[114:115], v[116:117], 0, s[18:19]
	global_load_lds_dwordx4 v[116:117], off
	v_min_i32_e32 v7, s17, v7
	s_mov_b32 m0, s26
	s_mov_b64 s[20:21], 0x30000
	v_lshl_add_u64 v[112:113], v[4:5], 0, v[2:3]
	global_load_lds_dwordx4 v[114:115], off
	v_add_u32_e32 v14, s16, v7
	s_mov_b32 m0, s27
	s_mov_b64 s[2:3], 0x80
	v_readfirstlane_b32 s24, v136
	v_lshl_add_u64 v[110:111], v[116:117], 0, s[20:21]
	global_load_lds_dwordx4 v[112:113], off
	v_ashrrev_i32_e32 v15, 31, v14
	s_mov_b32 m0, s28
	s_mov_b64 s[22:23], 0x10080
	v_add_u32_e32 v16, 0x4000, v136
	v_lshl_add_u64 v[4:5], v[116:117], 0, s[2:3]
	global_load_lds_dwordx4 v[110:111], off
	v_lshl_add_u64 v[14:15], v[14:15], 2, s[8:9]
	s_mov_b32 m0, s24
	v_lshl_add_u64 v[10:11], v[116:117], 0, s[22:23]
	global_load_lds_dwordx4 v[4:5], off
	s_mov_b32 m0, s14
	v_readfirstlane_b32 s6, v16
	global_load_lds_dwordx4 v[10:11], off
	s_mov_b32 m0, s6
	s_mov_b64 s[6:7], 0x30080
	v_add_u32_e32 v5, 0x6000, v136
	v_lshl_add_u64 v[12:13], v[112:113], 0, s[2:3]
	v_lshl_add_u64 v[10:11], v[116:117], 0, s[6:7]
	v_readfirstlane_b32 s6, v5
	global_load_lds_dwordx4 v[12:13], off
	s_mov_b32 m0, s6
	v_readfirstlane_b32 s6, v135
	v_add_u32_e32 v5, 0x2000, v135
	global_load_lds_dwordx4 v[10:11], off
	s_waitcnt vmcnt(8)
	v_mov_b32_e32 v4, v152
	v_ashrrev_i32_e32 v7, 31, v6
	v_lshlrev_b64 v[6:7], 10, v[6:7]
	v_ashrrev_i32_e32 v9, 31, v8
	v_lshl_add_u64 v[6:7], s[4:5], 0, v[6:7]
	v_lshl_add_u64 v[120:121], v[6:7], 0, v[2:3]
	v_lshlrev_b64 v[6:7], 10, v[8:9]
	v_lshl_add_u64 v[6:7], s[4:5], 0, v[6:7]
	s_mov_b32 m0, s6
	v_readfirstlane_b32 s6, v5
	v_lshl_add_u64 v[118:119], v[6:7], 0, v[2:3]
	global_load_lds_dwordx4 v[120:121], off
	s_mov_b32 m0, s6
	s_lshr_b32 s6, s34, 3
	global_load_lds_dwordx4 v[118:119], off
	v_readfirstlane_b32 s27, v0
	s_and_b32 s6, s6, 0x1ffffffe
	s_lshr_b32 s26, s27, 6
	s_add_i32 s6, s6, -16
	s_cmp_lt_i32 s26, s6
	v_ashrrev_i32_e32 v5, 31, v4
	v_lshlrev_b64 v[4:5], 10, v[4:5]
	v_lshl_add_u64 v[4:5], s[4:5], 0, v[4:5]
	s_cselect_b64 s[4:5], -1, 0
	s_cmp_ge_i32 s26, s6
	s_cselect_b64 s[30:31], -1, 0
	v_lshl_add_u64 v[122:123], v[4:5], 0, v[2:3]
	s_and_b64 vcc, exec, s[30:31]
	s_cbranch_vccnz .LBB4_37
	v_add_u32_e32 v2, 0x4000, v135
	s_nop 0
	v_readfirstlane_b32 s6, v2
	s_mov_b32 m0, s6
	s_nop 0
	global_load_lds_dwordx4 v[122:123], off

	.amdhsa_kernel _Z8moe_gemmILi2EEvPKDF16_S1_PvPKyPKiPKfS1_
		.amdhsa_group_segment_fixed_size 0
		.amdhsa_private_segment_fixed_size 0
		.amdhsa_kernarg_size 56
		.amdhsa_user_sgpr_count 2
		.amdhsa_user_sgpr_dispatch_ptr 0
		.amdhsa_user_sgpr_queue_ptr 0
		.amdhsa_user_sgpr_kernarg_segment_ptr 1
		.amdhsa_user_sgpr_dispatch_id 0
		.amdhsa_user_sgpr_kernarg_preload_length 0
		.amdhsa_user_sgpr_kernarg_preload_offset 0
		.amdhsa_user_sgpr_private_segment_size 0
		.amdhsa_uses_dynamic_stack 0
		.amdhsa_enable_private_segment 0
		.amdhsa_system_sgpr_workgroup_id_x 1
		.amdhsa_system_sgpr_workgroup_id_y 0
		.amdhsa_system_sgpr_workgroup_id_z 0
		.amdhsa_system_sgpr_workgroup_info 0
		.amdhsa_system_vgpr_workitem_id 0
		.amdhsa_next_free_vgpr 156
		.amdhsa_next_free_sgpr 62
		.amdhsa_accum_offset 156
		.amdhsa_reserve_vcc 1
		.amdhsa_float_round_mode_32 0
		.amdhsa_float_round_mode_16_64 0
		.amdhsa_float_denorm_mode_32 3
		.amdhsa_float_denorm_mode_16_64 3
		.amdhsa_dx10_clamp 1
		.amdhsa_ieee_mode 1
		.amdhsa_fp16_overflow 0
		.amdhsa_tg_split 0
		.amdhsa_exception_fp_ieee_invalid_op 0
		.amdhsa_exception_fp_denorm_src 0
		.amdhsa_exception_fp_ieee_div_zero 0
		.amdhsa_exception_fp_ieee_overflow 0
		.amdhsa_exception_fp_ieee_underflow 0
		.amdhsa_exception_fp_ieee_inexact 0
		.amdhsa_exception_int_div_zero 0
	.end_amdhsa_kernel

amdhsa.kernels:
  - .agpr_count:     0
    .args:
      - .actual_access:  write_only
        .address_space:  global
        .offset:         0
        .size:           8
        .value_kind:     global_buffer
    .group_segment_fixed_size: 0
    .kernarg_segment_align: 8
    .kernarg_segment_size: 8
    .language:       OpenCL C
    .language_version:
      - 2
      - 0
    .max_flat_workgroup_size: 1024
    .name:           _Z15zero_cnt_kernelPy
    .private_segment_fixed_size: 0
    .sgpr_count:     10
    .sgpr_spill_count: 0
    .symbol:         _Z15zero_cnt_kernelPy.kd
    .uniform_work_group_size: 1
    .uses_dynamic_stack: false
    .vgpr_count:     3
    .vgpr_spill_count: 0
    .wavefront_size: 64
  - .agpr_count:     0
    .args:
      - .actual_access:  read_only
        .address_space:  global
        .offset:         0
        .size:           8
        .value_kind:     global_buffer
      - .actual_access:  read_only
        .address_space:  global
        .offset:         8
        .size:           8
        .value_kind:     global_buffer
      - .actual_access:  read_only
        .address_space:  global
        .offset:         16
        .size:           8
        .value_kind:     global_buffer
      - .actual_access:  read_only
        .address_space:  global
        .offset:         24
        .size:           8
        .value_kind:     global_buffer
      - .actual_access:  write_only
        .address_space:  global
        .offset:         32
        .size:           8
        .value_kind:     global_buffer
      - .actual_access:  write_only
        .address_space:  global
        .offset:         40
        .size:           8
        .value_kind:     global_buffer
      - .actual_access:  write_only
        .address_space:  global
        .offset:         48
        .size:           8
        .value_kind:     global_buffer
      - .address_space:  global
        .offset:         56
        .size:           8
        .value_kind:     global_buffer
      - .actual_access:  write_only
        .address_space:  global
        .offset:         64
        .size:           8
        .value_kind:     global_buffer
      - .actual_access:  write_only
        .address_space:  global
        .offset:         72
        .size:           8
        .value_kind:     global_buffer
    .group_segment_fixed_size: 0
    .kernarg_segment_align: 8
    .kernarg_segment_size: 80
    .language:       OpenCL C
    .language_version:
      - 2
      - 0
    .max_flat_workgroup_size: 256
    .name:           _Z11prep_kernelPKfS0_S0_S0_PDF16_S1_S1_PyPiPf
    .private_segment_fixed_size: 0
    .sgpr_count:     55
    .sgpr_spill_count: 0
    .symbol:         _Z11prep_kernelPKfS0_S0_S0_PDF16_S1_S1_PyPiPf.kd
    .uniform_work_group_size: 1
    .uses_dynamic_stack: false
    .vgpr_count:     248
    .vgpr_spill_count: 0
    .wavefront_size: 64
  - .agpr_count:     0
    .args:
      - .address_space:  global
        .offset:         0
        .size:           8
        .value_kind:     global_buffer
      - .address_space:  global
        .offset:         8
        .size:           8
        .value_kind:     global_buffer
      - .actual_access:  write_only
        .address_space:  global
        .offset:         16
        .size:           8
        .value_kind:     global_buffer
      - .actual_access:  read_only
        .address_space:  global
        .offset:         24
        .size:           8
        .value_kind:     global_buffer
      - .actual_access:  read_only
        .address_space:  global
        .offset:         32
        .size:           8
        .value_kind:     global_buffer
      - .actual_access:  read_only
        .address_space:  global
        .offset:         40
        .size:           8
        .value_kind:     global_buffer
      - .actual_access:  read_only
        .address_space:  global
        .offset:         48
        .size:           8
        .value_kind:     global_buffer
    .group_segment_fixed_size: 0
    .kernarg_segment_align: 8
    .kernarg_segment_size: 56
    .language:       OpenCL C
    .language_version:
      - 2
      - 0
    .max_flat_workgroup_size: 512
    .name:           _Z8moe_gemmILi0EEvPKDF16_S1_PvPKyPKiPKfS1_
    .private_segment_fixed_size: 0
    .sgpr_count:     82
    .sgpr_spill_count: 0
    .symbol:         _Z8moe_gemmILi0EEvPKDF16_S1_PvPKyPKiPKfS1_.kd
    .uniform_work_group_size: 1
    .uses_dynamic_stack: false
    .vgpr_count:     248
    .vgpr_spill_count: 0
    .wavefront_size: 64
  - .agpr_count:     0
    .args:
      - .address_space:  global
        .offset:         0
        .size:           8
        .value_kind:     global_buffer
      - .address_space:  global
        .offset:         8
        .size:           8
        .value_kind:     global_buffer
      - .actual_access:  write_only
        .address_space:  global
        .offset:         16
        .size:           8
        .value_kind:     global_buffer
      - .actual_access:  read_only
        .address_space:  global
        .offset:         24
        .size:           8
        .value_kind:     global_buffer
      - .actual_access:  read_only
        .address_space:  global
        .offset:         32
        .size:           8
        .value_kind:     global_buffer
      - .actual_access:  read_only
        .address_space:  global
        .offset:         40
        .size:           8
        .value_kind:     global_buffer
      - .actual_access:  read_only
        .address_space:  global
        .offset:         48
        .size:           8
        .value_kind:     global_buffer
    .group_segment_fixed_size: 0
    .kernarg_segment_align: 8
    .kernarg_segment_size: 56
    .language:       OpenCL C
    .language_version:
      - 2
      - 0
    .max_flat_workgroup_size: 512
    .name:           _Z8moe_gemmILi1EEvPKDF16_S1_PvPKyPKiPKfS1_
    .private_segment_fixed_size: 0
    .sgpr_count:     68
    .sgpr_spill_count: 0
    .symbol:         _Z8moe_gemmILi1EEvPKDF16_S1_PvPKyPKiPKfS1_.kd
    .uniform_work_group_size: 1
    .uses_dynamic_stack: false
    .vgpr_count:     148
    .vgpr_spill_count: 0
    .wavefront_size: 64
  - .agpr_count:     0
    .args:
      - .address_space:  global
        .offset:         0
        .size:           8
        .value_kind:     global_buffer
      - .address_space:  global
        .offset:         8
        .size:           8
        .value_kind:     global_buffer
      - .actual_access:  write_only
        .address_space:  global
        .offset:         16
        .size:           8
        .value_kind:     global_buffer
      - .actual_access:  read_only
        .address_space:  global
        .offset:         24
        .size:           8
        .value_kind:     global_buffer
      - .actual_access:  read_only
        .address_space:  global
        .offset:         32
        .size:           8
        .value_kind:     global_buffer
      - .actual_access:  read_only
        .address_space:  global
        .offset:         40
        .size:           8
        .value_kind:     global_buffer
      - .actual_access:  read_only
        .address_space:  global
        .offset:         48
        .size:           8
        .value_kind:     global_buffer
    .group_segment_fixed_size: 0
    .kernarg_segment_align: 8
    .kernarg_segment_size: 56
    .language:       OpenCL C
    .language_version:
      - 2
      - 0
    .max_flat_workgroup_size: 512
    .name:           _Z8moe_gemmILi2EEvPKDF16_S1_PvPKyPKiPKfS1_
    .private_segment_fixed_size: 0
    .sgpr_count:     68
    .sgpr_spill_count: 0
    .symbol:         _Z8moe_gemmILi2EEvPKDF16_S1_PvPKyPKiPKfS1_.kd
    .uniform_work_group_size: 1
    .uses_dynamic_stack: false
    .vgpr_count:     156
    .vgpr_spill_count: 0
    .wavefront_size: 64
